# phase F layer 0: the 8 row loads issued together (sum-of-squares temporaries renamed into free VGPRs, counted waits re-derived) instead of hipcc's 2+4+2 groups
# speedup vs baseline: 1.0077x; 1.0029x over previous
.LBB0_1365:
	s_cmp_lg_u32 s1, -1
	s_cselect_b32 s52, s1, 0
	s_cselect_b32 s53, s43, 0
	s_cmp_lg_u32 s45, -1
	s_cselect_b32 s61, s45, 0
	s_cselect_b32 s62, s43, 0
	s_cmpk_lt_i32 s0, 0x4000
	s_cselect_b32 s53, s53, s42
	s_cselect_b32 s52, s52, s33
	s_waitcnt vmcnt(7) lgkmcnt(7)
	v_lshl_add_u64 v[18:19], s[40:41], 0, v[110:111]
	v_lshl_add_u64 v[118:119], s[52:53], 0, v[112:113]
	s_mov_b32 s52, 0x1b41000
	v_add_co_u32_e32 v14, vcc, s52, v18
	ds_read_b128 v[86:89], v134
	ds_read_b128 v[82:85], v134 offset:8192
	ds_read_b128 v[78:81], v134 offset:16384
	ds_read_b128 v[74:77], v134 offset:24576
	ds_read_b128 v[70:73], v134 offset:32768
	ds_read_b128 v[66:69], v134 offset:40960
	ds_read_b128 v[62:65], v134 offset:49152
	ds_read_b128 v[58:61], v134 offset:57344
	ds_read_b128 v[54:57], v135
	ds_read_b128 v[50:53], v136
	ds_read_b128 v[46:49], v137
	ds_read_b128 v[42:45], v138
	ds_read_b128 v[38:41], v139
	ds_read_b128 v[34:37], v140
	s_waitcnt vmcnt(4) lgkmcnt(14)
	ds_read_b128 v[30:33], v141
	ds_read_b128 v[26:29], v142
	v_addc_co_u32_e32 v15, vcc, 0, v19, vcc
	global_load_dwordx4 v[2:5], v[14:15], off offset:3072
	global_load_dwordx4 v[6:9], v[14:15], off offset:2048
	s_mov_b32 s52, 0x1b40000
	v_add_co_u32_e32 v94, vcc, s52, v18
	s_cselect_b32 s63, s62, s55
	s_nop 0
	v_addc_co_u32_e32 v95, vcc, 0, v19, vcc
	global_load_dwordx4 v[10:13], v[14:15], off offset:1024
	s_nop 0
	global_load_dwordx4 v[14:17], v[14:15], off
	global_load_dwordx4 v[90:93], v[94:95], off offset:1024
	global_load_dwordx4 v[102:105], v[94:95], off
	global_load_dwordx4 v[18:21], v[94:95], off offset:3072
	global_load_dwordx4 v[22:25], v[94:95], off offset:2048
	s_cselect_b32 s62, s61, s54
	v_lshl_add_u64 v[116:117], s[62:63], 0, v[112:113]
	s_mov_b32 s52, 0x800000
	v_lshl_add_u64 v[120:121], s[40:41], 0, v[108:109]
	s_waitcnt vmcnt(7)
	v_mov_b32_e32 v221, v3
	s_waitcnt vmcnt(6)
	v_mov_b32_e32 v220, v7
	v_mov_b32_e32 v218, v6
	v_mov_b32_e32 v219, v2
	v_pk_mul_f32 v[220:221], v[220:221], v[220:221]
	s_nop 0
	v_pk_fma_f32 v[218:219], v[218:219], v[218:219], v[220:221]
	v_mov_b32_e32 v220, v8
	v_mov_b32_e32 v221, v4
	v_pk_fma_f32 v[218:219], v[220:221], v[220:221], v[218:219]
	v_mov_b32_e32 v220, v9
	v_mov_b32_e32 v221, v5
	v_pk_fma_f32 v[114:115], v[220:221], v[220:221], v[218:219]
	ds_read_b128 v[98:101], v133
	s_waitcnt vmcnt(5)
	v_mov_b32_e32 v225, v11
	s_waitcnt vmcnt(4)
	v_mov_b32_e32 v224, v15
	v_mov_b32_e32 v222, v14
	v_mov_b32_e32 v223, v10
	v_pk_mul_f32 v[224:225], v[224:225], v[224:225]
	s_waitcnt vmcnt(3)
	v_mul_f32_e32 v215, v91, v91
	v_pk_fma_f32 v[222:223], v[222:223], v[222:223], v[224:225]
	v_mov_b32_e32 v224, v16
	v_mov_b32_e32 v225, v12
	v_pk_fma_f32 v[222:223], v[224:225], v[224:225], v[222:223]
	v_mov_b32_e32 v224, v17
	v_mov_b32_e32 v225, v13
	v_pk_fma_f32 v[124:125], v[224:225], v[224:225], v[222:223]
	s_nop 0
	flat_load_dwordx4 v[94:97], v[118:119]
	flat_load_dwordx4 v[210:213], v[116:117]
	s_waitcnt vmcnt(0)
	v_mul_f32_e32 v216, v103, v103
	v_fmac_f32_e32 v215, v90, v90
	v_fmac_f32_e32 v216, v102, v102
	v_fmac_f32_e32 v215, v92, v92
	v_fmac_f32_e32 v216, v104, v104
	v_fmac_f32_e32 v215, v93, v93
	v_fmac_f32_e32 v216, v105, v105
	v_mul_f32_e32 v190, v19, v19
	v_mul_f32_e32 v214, v23, v23
	v_fmac_f32_e32 v214, v22, v22
	v_fmac_f32_e32 v190, v18, v18
	v_fmac_f32_e32 v214, v24, v24
	v_fmac_f32_e32 v190, v20, v20
	v_fmac_f32_e32 v214, v25, v25
	s_waitcnt lgkmcnt(0)
	v_mov_b32_e32 v122, v210
	v_add_f32_e32 v210, v216, v215
	v_fmac_f32_e32 v190, v21, v21
	v_add_f32_e32 v210, v210, v214
	v_add_f32_e32 v190, v210, v190
	v_add_f32_e32 v124, v190, v124
	v_add_f32_e32 v124, v124, v125
	v_add_f32_e32 v114, v124, v114
	v_add_f32_e32 v114, v114, v115
	ds_bpermute_b32 v115, v1, v114
	v_mov_b32_e32 v124, v102
	v_mov_b32_e32 v125, v104
	v_mov_b32_e32 v104, v103
	v_mov_b32_e32 v123, v212
	s_waitcnt lgkmcnt(0)
	v_add_f32_e32 v114, v114, v115
	ds_bpermute_b32 v115, v128, v114
	v_mov_b32_e32 v212, v211
	v_mov_b32_e32 v210, v98
	v_mov_b32_e32 v211, v100
	v_mov_b32_e32 v100, v99
	s_waitcnt lgkmcnt(0)
	v_add_f32_e32 v114, v114, v115
	ds_bpermute_b32 v115, v129, v114
	v_pk_add_f32 v[126:127], v[122:123], 1.0 op_sel_hi:[1,0]
	v_pk_add_f32 v[122:123], v[212:213], 1.0 op_sel_hi:[1,0]
	s_waitcnt lgkmcnt(0)
	v_add_f32_e32 v114, v114, v115
	ds_bpermute_b32 v115, v130, v114
	s_waitcnt lgkmcnt(0)
	v_add_f32_e32 v114, v114, v115
	ds_bpermute_b32 v115, v131, v114
	s_waitcnt lgkmcnt(0)
	v_add_f32_e32 v114, v114, v115
	ds_bpermute_b32 v115, v132, v114
	s_waitcnt lgkmcnt(0)
	v_add_f32_e32 v114, v114, v115
	v_fmamk_f32 v114, v114, 0x3a000000, v207
	v_cmp_gt_f32_e32 vcc, s52, v114
	v_mul_f32_e32 v115, 0x4b800000, v114
	s_mov_b32 s52, 0x2ec40000
	v_cndmask_b32_e32 v114, v114, v115, vcc
	v_rsq_f32_e32 v114, v114
	s_nop 0
	v_mul_f32_e32 v115, 0x45800000, v114
	v_cndmask_b32_e32 v114, v114, v115, vcc
	v_pk_mul_f32 v[124:125], v[124:125], v[114:115] op_sel_hi:[1,0]
	v_pk_mul_f32 v[102:103], v[104:105], v[114:115] op_sel_hi:[1,0]
	v_pk_mul_f32 v[124:125], v[210:211], v[124:125]
	v_mov_b32_e32 v211, v96
	v_pk_mul_f32 v[98:99], v[100:101], v[102:103]
	v_mov_b32_e32 v96, v95
	v_mov_b32_e32 v210, v94
	v_pk_fma_f32 v[96:97], v[122:123], v[98:99], v[96:97]
	v_pk_fma_f32 v[124:125], v[126:127], v[124:125], v[210:211]
	v_fma_f32 v33, v97, v33, 0
	v_fmac_f32_e32 v33, v125, v32
	v_and_b32_sdwa v98, v97, v208 dst_sel:DWORD dst_unused:UNUSED_PAD src0_sel:WORD_1 src1_sel:DWORD
	v_fmac_f32_e32 v33, v96, v31
	v_and_b32_sdwa v94, v125, v208 dst_sel:DWORD dst_unused:UNUSED_PAD src0_sel:WORD_1 src1_sel:DWORD
	v_and_b32_sdwa v99, v96, v208 dst_sel:DWORD dst_unused:UNUSED_PAD src0_sel:WORD_1 src1_sel:DWORD
	v_add3_u32 v98, v97, v98, s57
	v_fmac_f32_e32 v33, v124, v30
	v_fma_f32 v30, v97, v29, 0
	v_and_b32_sdwa v95, v124, v208 dst_sel:DWORD dst_unused:UNUSED_PAD src0_sel:WORD_1 src1_sel:DWORD
	v_add3_u32 v94, v125, v94, s57
	v_add3_u32 v99, v96, v99, s57
	v_and_b32_e32 v98, 0xffff0000, v98
	v_fma_f32 v89, v97, v89, 0
	v_fma_f32 v85, v97, v85, 0
	v_fma_f32 v81, v97, v81, 0
	v_fma_f32 v77, v97, v77, 0
	v_fma_f32 v73, v97, v73, 0
	v_fma_f32 v69, v97, v69, 0
	v_fma_f32 v65, v97, v65, 0
	v_fma_f32 v61, v97, v61, 0
	v_fma_f32 v57, v97, v57, 0
	v_fma_f32 v53, v97, v53, 0
	v_fma_f32 v49, v97, v49, 0
	v_fma_f32 v45, v97, v45, 0
	v_fma_f32 v41, v97, v41, 0
	v_fma_f32 v37, v97, v37, 0
	v_fmac_f32_e32 v30, v125, v28
	v_add3_u32 v95, v124, v95, s57
	v_and_b32_e32 v100, 0xffff0000, v99
	v_or_b32_sdwa v99, v98, v94 dst_sel:DWORD dst_unused:UNUSED_PAD src0_sel:DWORD src1_sel:WORD_1
	v_add_co_u32_e32 v94, vcc, s52, v120
	v_fmac_f32_e32 v89, v125, v88
	v_fmac_f32_e32 v85, v125, v84
	v_fmac_f32_e32 v81, v125, v80
	v_fmac_f32_e32 v77, v125, v76
	v_fmac_f32_e32 v73, v125, v72
	v_fmac_f32_e32 v69, v125, v68
	v_fmac_f32_e32 v65, v125, v64
	v_fmac_f32_e32 v61, v125, v60
	v_fmac_f32_e32 v57, v125, v56
	v_fmac_f32_e32 v53, v125, v52
	v_fmac_f32_e32 v49, v125, v48
	v_fmac_f32_e32 v45, v125, v44
	v_fmac_f32_e32 v41, v125, v40
	v_fmac_f32_e32 v37, v125, v36
	v_fmac_f32_e32 v30, v96, v27
	v_or_b32_sdwa v98, v100, v95 dst_sel:DWORD dst_unused:UNUSED_PAD src0_sel:DWORD src1_sel:WORD_1
	v_addc_co_u32_e32 v95, vcc, 0, v121, vcc
	v_fmac_f32_e32 v89, v96, v87
	v_fmac_f32_e32 v85, v96, v83
	v_fmac_f32_e32 v81, v96, v79
	v_fmac_f32_e32 v77, v96, v75
	v_fmac_f32_e32 v73, v96, v71
	v_fmac_f32_e32 v69, v96, v67
	v_fmac_f32_e32 v65, v96, v63
	v_fmac_f32_e32 v61, v96, v59
	v_fmac_f32_e32 v57, v96, v55
	v_fmac_f32_e32 v53, v96, v51
	v_fmac_f32_e32 v49, v96, v47
	v_fmac_f32_e32 v45, v96, v43
	v_fmac_f32_e32 v41, v96, v39
	v_fmac_f32_e32 v37, v96, v35
	v_fmac_f32_e32 v30, v124, v26
	global_store_dwordx2 v[94:95], v[98:99], off
	v_fmac_f32_e32 v89, v124, v86
	v_fmac_f32_e32 v85, v124, v82
	v_fmac_f32_e32 v81, v124, v78
	v_fmac_f32_e32 v77, v124, v74
	v_fmac_f32_e32 v73, v124, v70
	v_fmac_f32_e32 v69, v124, v66
	v_fmac_f32_e32 v65, v124, v62
	v_fmac_f32_e32 v61, v124, v58
	v_fmac_f32_e32 v57, v124, v54
	v_fmac_f32_e32 v53, v124, v50
	v_fmac_f32_e32 v49, v124, v46
	v_fmac_f32_e32 v45, v124, v42
	v_fmac_f32_e32 v41, v124, v38
	v_fmac_f32_e32 v37, v124, v34
	ds_read_b128 v[96:99], v143
	flat_load_dwordx4 v[100:103], v[118:119] offset:1024
	flat_load_dwordx4 v[120:123], v[116:117] offset:1024
	v_mov_b32_e32 v26, v90
	v_mov_b32_e32 v27, v92
	v_pk_mul_f32 v[26:27], v[26:27], v[114:115] op_sel_hi:[1,0]
	s_waitcnt lgkmcnt(0)
	v_mov_b32_e32 v28, v96
	v_mov_b32_e32 v29, v98
	v_pk_mul_f32 v[26:27], v[26:27], v[28:29]
	v_mov_b32_e32 v92, v91
	v_mov_b32_e32 v98, v97
	s_waitcnt vmcnt(0)
	v_mov_b32_e32 v34, v100
	v_mov_b32_e32 v28, v120
	v_mov_b32_e32 v29, v122
	v_pk_add_f32 v[28:29], v[28:29], 1.0 op_sel_hi:[1,0]
	v_mov_b32_e32 v35, v102
	v_pk_fma_f32 v[26:27], v[26:27], v[28:29], v[34:35]
	v_pk_mul_f32 v[28:29], v[92:93], v[114:115] op_sel_hi:[1,0]
	ds_read_b128 v[90:93], v134 offset:1024
	v_mov_b32_e32 v122, v121
	v_pk_mul_f32 v[28:29], v[28:29], v[98:99]
	v_pk_add_f32 v[34:35], v[122:123], 1.0 op_sel_hi:[1,0]
	v_mov_b32_e32 v102, v101
	v_pk_fma_f32 v[28:29], v[28:29], v[34:35], v[102:103]
	v_and_b32_sdwa v31, v27, v208 dst_sel:DWORD dst_unused:UNUSED_PAD src0_sel:WORD_1 src1_sel:DWORD
	s_waitcnt lgkmcnt(0)
	v_fmac_f32_e32 v89, v29, v93
	v_fmac_f32_e32 v89, v27, v92
	v_fmac_f32_e32 v89, v28, v91
	v_fmac_f32_e32 v89, v26, v90
	ds_read_b128 v[90:93], v134 offset:9216
	v_and_b32_sdwa v34, v29, v208 dst_sel:DWORD dst_unused:UNUSED_PAD src0_sel:WORD_1 src1_sel:DWORD
	v_and_b32_sdwa v35, v28, v208 dst_sel:DWORD dst_unused:UNUSED_PAD src0_sel:WORD_1 src1_sel:DWORD
	v_and_b32_sdwa v32, v26, v208 dst_sel:DWORD dst_unused:UNUSED_PAD src0_sel:WORD_1 src1_sel:DWORD
	v_add3_u32 v34, v29, v34, s57
	s_waitcnt lgkmcnt(0)
	v_fmac_f32_e32 v85, v29, v93
	v_fmac_f32_e32 v85, v27, v92
	v_fmac_f32_e32 v85, v28, v91
	v_fmac_f32_e32 v85, v26, v90
	ds_read_b128 v[90:93], v134 offset:17408
	v_add3_u32 v35, v28, v35, s57
	v_add3_u32 v32, v26, v32, s57
	v_add3_u32 v31, v27, v31, s57
	v_and_b32_e32 v34, 0xffff0000, v34
	s_waitcnt lgkmcnt(0)
	v_fmac_f32_e32 v81, v29, v93
	v_fmac_f32_e32 v81, v27, v92
	v_fmac_f32_e32 v81, v28, v91
	v_fmac_f32_e32 v81, v26, v90
	ds_read_b128 v[90:93], v134 offset:25600
	v_and_b32_e32 v36, 0xffff0000, v35
	v_or_b32_sdwa v35, v34, v31 dst_sel:DWORD dst_unused:UNUSED_PAD src0_sel:DWORD src1_sel:WORD_1
	v_or_b32_sdwa v34, v36, v32 dst_sel:DWORD dst_unused:UNUSED_PAD src0_sel:DWORD src1_sel:WORD_1
	global_store_dwordx2 v[94:95], v[34:35], off offset:512
	s_waitcnt lgkmcnt(0)
	v_fmac_f32_e32 v77, v29, v93
	v_fmac_f32_e32 v77, v27, v92
	v_fmac_f32_e32 v77, v28, v91
	v_fmac_f32_e32 v77, v26, v90
	ds_read_b128 v[90:93], v134 offset:33792
	s_waitcnt lgkmcnt(0)
	v_fmac_f32_e32 v73, v29, v93
	v_fmac_f32_e32 v73, v27, v92
	v_fmac_f32_e32 v73, v28, v91
	v_fmac_f32_e32 v73, v26, v90
	ds_read_b128 v[90:93], v134 offset:41984
	s_waitcnt lgkmcnt(0)
	v_fmac_f32_e32 v69, v29, v93
	v_fmac_f32_e32 v69, v27, v92
	v_fmac_f32_e32 v69, v28, v91
	v_fmac_f32_e32 v69, v26, v90
	ds_read_b128 v[90:93], v134 offset:50176
	s_waitcnt lgkmcnt(0)
	v_fmac_f32_e32 v65, v29, v93
	v_fmac_f32_e32 v65, v27, v92
	v_fmac_f32_e32 v65, v28, v91
	v_fmac_f32_e32 v65, v26, v90
	ds_read_b128 v[90:93], v134 offset:58368
	s_waitcnt lgkmcnt(0)
	v_fmac_f32_e32 v61, v29, v93
	v_fmac_f32_e32 v61, v27, v92
	v_fmac_f32_e32 v61, v28, v91
	v_fmac_f32_e32 v61, v26, v90
	ds_read_b128 v[90:93], v144
	s_waitcnt lgkmcnt(0)
	v_fmac_f32_e32 v57, v29, v93
	v_fmac_f32_e32 v57, v27, v92
	v_fmac_f32_e32 v57, v28, v91
	v_fmac_f32_e32 v57, v26, v90
	ds_read_b128 v[90:93], v145
	s_waitcnt lgkmcnt(0)
	v_fmac_f32_e32 v53, v29, v93
	v_fmac_f32_e32 v53, v27, v92
	v_fmac_f32_e32 v53, v28, v91
	v_fmac_f32_e32 v53, v26, v90
	ds_read_b128 v[90:93], v146
	s_waitcnt lgkmcnt(0)
	v_fmac_f32_e32 v49, v29, v93
	v_fmac_f32_e32 v49, v27, v92
	v_fmac_f32_e32 v49, v28, v91
	v_fmac_f32_e32 v49, v26, v90
	ds_read_b128 v[90:93], v147
	s_waitcnt lgkmcnt(0)
	v_fmac_f32_e32 v45, v29, v93
	v_fmac_f32_e32 v45, v27, v92
	v_fmac_f32_e32 v45, v28, v91
	v_fmac_f32_e32 v45, v26, v90
	ds_read_b128 v[90:93], v148
	s_waitcnt lgkmcnt(0)
	v_fmac_f32_e32 v41, v29, v93
	v_fmac_f32_e32 v41, v27, v92
	v_fmac_f32_e32 v41, v28, v91
	v_fmac_f32_e32 v41, v26, v90
	ds_read_b128 v[90:93], v149
	s_waitcnt lgkmcnt(0)
	v_fmac_f32_e32 v37, v29, v93
	v_fmac_f32_e32 v37, v27, v92
	v_fmac_f32_e32 v37, v28, v91
	v_fmac_f32_e32 v37, v26, v90
	ds_read_b128 v[90:93], v150
	s_waitcnt lgkmcnt(0)
	v_fmac_f32_e32 v33, v29, v93
	v_fmac_f32_e32 v33, v27, v92
	v_fmac_f32_e32 v33, v28, v91
	v_fmac_f32_e32 v33, v26, v90
	ds_read_b128 v[90:93], v151
	s_waitcnt lgkmcnt(0)
	v_fmac_f32_e32 v30, v29, v93
	v_fmac_f32_e32 v30, v27, v92
	v_fmac_f32_e32 v30, v28, v91
	v_fmac_f32_e32 v30, v26, v90
	ds_read_b128 v[90:93], v152
	flat_load_dwordx4 v[96:99], v[118:119] offset:2048
	flat_load_dwordx4 v[100:103], v[116:117] offset:2048
	v_mov_b32_e32 v27, v24
	v_mov_b32_e32 v24, v23
	v_mov_b32_e32 v26, v22
	s_waitcnt lgkmcnt(0)
	v_mov_b32_e32 v29, v92
	v_pk_mul_f32 v[22:23], v[24:25], v[114:115] op_sel_hi:[1,0]
	v_mov_b32_e32 v92, v91
	v_mov_b32_e32 v28, v90
	v_pk_mul_f32 v[22:23], v[22:23], v[92:93]
	ds_read_b128 v[90:93], v134 offset:2048
	v_pk_mul_f32 v[26:27], v[26:27], v[114:115] op_sel_hi:[1,0]
	s_waitcnt vmcnt(0)
	v_mov_b32_e32 v35, v98
	v_pk_mul_f32 v[26:27], v[26:27], v[28:29]
	v_mov_b32_e32 v29, v102
	v_mov_b32_e32 v102, v101
	v_mov_b32_e32 v28, v100
	v_pk_add_f32 v[24:25], v[102:103], 1.0 op_sel_hi:[1,0]
	v_mov_b32_e32 v98, v97
	v_pk_add_f32 v[28:29], v[28:29], 1.0 op_sel_hi:[1,0]
	v_mov_b32_e32 v34, v96
	v_pk_fma_f32 v[22:23], v[22:23], v[24:25], v[98:99]
	v_pk_fma_f32 v[26:27], v[26:27], v[28:29], v[34:35]
	s_waitcnt lgkmcnt(0)
	v_fmac_f32_e32 v89, v23, v93
	v_fmac_f32_e32 v89, v27, v92
	v_fmac_f32_e32 v89, v22, v91
	v_fmac_f32_e32 v89, v26, v90
	ds_read_b128 v[90:93], v134 offset:10240
	v_and_b32_sdwa v25, v26, v208 dst_sel:DWORD dst_unused:UNUSED_PAD src0_sel:WORD_1 src1_sel:DWORD
	v_add3_u32 v28, v26, v25, s57
	v_and_b32_sdwa v25, v23, v208 dst_sel:DWORD dst_unused:UNUSED_PAD src0_sel:WORD_1 src1_sel:DWORD
	v_and_b32_sdwa v29, v22, v208 dst_sel:DWORD dst_unused:UNUSED_PAD src0_sel:WORD_1 src1_sel:DWORD
	s_waitcnt lgkmcnt(0)
	v_fmac_f32_e32 v85, v23, v93
	v_fmac_f32_e32 v85, v27, v92
	v_fmac_f32_e32 v85, v22, v91
	v_fmac_f32_e32 v85, v26, v90
	ds_read_b128 v[90:93], v134 offset:18432
	v_and_b32_sdwa v24, v27, v208 dst_sel:DWORD dst_unused:UNUSED_PAD src0_sel:WORD_1 src1_sel:DWORD
	v_add3_u32 v25, v23, v25, s57
	v_add3_u32 v29, v22, v29, s57
	v_add3_u32 v24, v27, v24, s57
	s_waitcnt lgkmcnt(0)
	v_fmac_f32_e32 v81, v23, v93
	v_fmac_f32_e32 v81, v27, v92
	v_fmac_f32_e32 v81, v22, v91
	v_fmac_f32_e32 v81, v26, v90
	ds_read_b128 v[90:93], v134 offset:26624
	v_and_b32_e32 v25, 0xffff0000, v25
	v_and_b32_e32 v29, 0xffff0000, v29
	v_or_b32_sdwa v25, v25, v24 dst_sel:DWORD dst_unused:UNUSED_PAD src0_sel:DWORD src1_sel:WORD_1
	v_or_b32_sdwa v24, v29, v28 dst_sel:DWORD dst_unused:UNUSED_PAD src0_sel:DWORD src1_sel:WORD_1
	s_waitcnt lgkmcnt(0)
	v_fmac_f32_e32 v77, v23, v93
	v_fmac_f32_e32 v77, v27, v92
	v_fmac_f32_e32 v77, v22, v91
	v_fmac_f32_e32 v77, v26, v90
	ds_read_b128 v[90:93], v134 offset:34816
	global_store_dwordx2 v[94:95], v[24:25], off offset:1024
	s_waitcnt lgkmcnt(0)
	v_fmac_f32_e32 v73, v23, v93
	v_fmac_f32_e32 v73, v27, v92
	v_fmac_f32_e32 v73, v22, v91
	v_fmac_f32_e32 v73, v26, v90
	ds_read_b128 v[90:93], v134 offset:43008
	s_waitcnt lgkmcnt(0)
	v_fmac_f32_e32 v69, v23, v93
	v_fmac_f32_e32 v69, v27, v92
	v_fmac_f32_e32 v69, v22, v91
	v_fmac_f32_e32 v69, v26, v90
	ds_read_b128 v[90:93], v134 offset:51200
	s_waitcnt lgkmcnt(0)
	v_fmac_f32_e32 v65, v23, v93
	v_fmac_f32_e32 v65, v27, v92
	v_fmac_f32_e32 v65, v22, v91
	v_fmac_f32_e32 v65, v26, v90
	ds_read_b128 v[90:93], v134 offset:59392
	s_waitcnt lgkmcnt(0)
	v_fmac_f32_e32 v61, v23, v93
	v_fmac_f32_e32 v61, v27, v92
	v_fmac_f32_e32 v61, v22, v91
	v_fmac_f32_e32 v61, v26, v90
	ds_read_b128 v[90:93], v153
	s_waitcnt lgkmcnt(0)
	v_fmac_f32_e32 v57, v23, v93
	v_fmac_f32_e32 v57, v27, v92
	v_fmac_f32_e32 v57, v22, v91
	v_fmac_f32_e32 v57, v26, v90
	ds_read_b128 v[90:93], v154
	s_waitcnt lgkmcnt(0)
	v_fmac_f32_e32 v53, v23, v93
	v_fmac_f32_e32 v53, v27, v92
	v_fmac_f32_e32 v53, v22, v91
	v_fmac_f32_e32 v53, v26, v90
	ds_read_b128 v[90:93], v155
	s_waitcnt lgkmcnt(0)
	v_fmac_f32_e32 v49, v23, v93
	v_fmac_f32_e32 v49, v27, v92
	v_fmac_f32_e32 v49, v22, v91
	v_fmac_f32_e32 v49, v26, v90
	ds_read_b128 v[90:93], v156
	s_waitcnt lgkmcnt(0)
	v_fmac_f32_e32 v45, v23, v93
	v_fmac_f32_e32 v45, v27, v92
	v_fmac_f32_e32 v45, v22, v91
	v_fmac_f32_e32 v45, v26, v90
	ds_read_b128 v[90:93], v157
	s_waitcnt lgkmcnt(0)
	v_fmac_f32_e32 v41, v23, v93
	v_fmac_f32_e32 v41, v27, v92
	v_fmac_f32_e32 v41, v22, v91
	v_fmac_f32_e32 v41, v26, v90
	ds_read_b128 v[90:93], v158
	s_waitcnt lgkmcnt(0)
	v_fmac_f32_e32 v37, v23, v93
	v_fmac_f32_e32 v37, v27, v92
	v_fmac_f32_e32 v37, v22, v91
	v_fmac_f32_e32 v37, v26, v90
	ds_read_b128 v[90:93], v159
	s_waitcnt lgkmcnt(0)
	v_fmac_f32_e32 v33, v23, v93
	v_fmac_f32_e32 v33, v27, v92
	v_fmac_f32_e32 v33, v22, v91
	v_fmac_f32_e32 v33, v26, v90
	ds_read_b128 v[90:93], v160
	s_waitcnt lgkmcnt(0)
	v_fmac_f32_e32 v30, v23, v93
	v_fmac_f32_e32 v30, v27, v92
	v_fmac_f32_e32 v30, v22, v91
	v_fmac_f32_e32 v30, v26, v90
	ds_read_b128 v[24:27], v161
	flat_load_dwordx4 v[90:93], v[118:119] offset:3072
	flat_load_dwordx4 v[96:99], v[116:117] offset:3072
	v_mov_b32_e32 v22, v18
	v_mov_b32_e32 v23, v20
	v_pk_mul_f32 v[22:23], v[22:23], v[114:115] op_sel_hi:[1,0]
	s_waitcnt lgkmcnt(0)
	v_mov_b32_e32 v28, v24
	v_mov_b32_e32 v29, v26
	v_pk_mul_f32 v[22:23], v[22:23], v[28:29]
	v_mov_b32_e32 v20, v19
	v_pk_mul_f32 v[18:19], v[20:21], v[114:115] op_sel_hi:[1,0]
	v_mov_b32_e32 v26, v25
	v_pk_mul_f32 v[18:19], v[18:19], v[26:27]
	s_waitcnt vmcnt(0)
	v_mov_b32_e32 v34, v90
	v_mov_b32_e32 v28, v96
	v_mov_b32_e32 v29, v98
	v_pk_add_f32 v[28:29], v[28:29], 1.0 op_sel_hi:[1,0]
	v_mov_b32_e32 v35, v92
	v_mov_b32_e32 v98, v97
	v_pk_fma_f32 v[22:23], v[22:23], v[28:29], v[34:35]
	v_pk_add_f32 v[20:21], v[98:99], 1.0 op_sel_hi:[1,0]
	v_mov_b32_e32 v92, v91
	v_pk_fma_f32 v[18:19], v[18:19], v[20:21], v[92:93]
	v_and_b32_sdwa v21, v22, v208 dst_sel:DWORD dst_unused:UNUSED_PAD src0_sel:WORD_1 src1_sel:DWORD
	v_add3_u32 v24, v22, v21, s57
	v_and_b32_sdwa v21, v19, v208 dst_sel:DWORD dst_unused:UNUSED_PAD src0_sel:WORD_1 src1_sel:DWORD
	v_and_b32_sdwa v25, v18, v208 dst_sel:DWORD dst_unused:UNUSED_PAD src0_sel:WORD_1 src1_sel:DWORD
	v_and_b32_sdwa v20, v23, v208 dst_sel:DWORD dst_unused:UNUSED_PAD src0_sel:WORD_1 src1_sel:DWORD
	v_add3_u32 v21, v19, v21, s57
	v_add3_u32 v25, v18, v25, s57
	v_add3_u32 v20, v23, v20, s57
	v_and_b32_e32 v21, 0xffff0000, v21
	v_and_b32_e32 v25, 0xffff0000, v25
	v_or_b32_sdwa v21, v21, v20 dst_sel:DWORD dst_unused:UNUSED_PAD src0_sel:DWORD src1_sel:WORD_1
	v_or_b32_sdwa v20, v25, v24 dst_sel:DWORD dst_unused:UNUSED_PAD src0_sel:DWORD src1_sel:WORD_1
	ds_read_b128 v[24:27], v134 offset:3072
	global_store_dwordx2 v[94:95], v[20:21], off offset:1536
	s_waitcnt lgkmcnt(0)
	v_fmac_f32_e32 v89, v19, v27
	v_fmac_f32_e32 v89, v23, v26
	v_fmac_f32_e32 v89, v18, v25
	v_fmac_f32_e32 v89, v22, v24
	ds_read_b128 v[24:27], v134 offset:11264
	s_waitcnt lgkmcnt(0)
	v_fmac_f32_e32 v85, v19, v27
	v_fmac_f32_e32 v85, v23, v26
	v_fmac_f32_e32 v85, v18, v25
	v_fmac_f32_e32 v85, v22, v24
	ds_read_b128 v[24:27], v134 offset:19456
	s_waitcnt lgkmcnt(0)
	v_fmac_f32_e32 v81, v19, v27
	v_fmac_f32_e32 v81, v23, v26
	v_fmac_f32_e32 v81, v18, v25
	v_fmac_f32_e32 v81, v22, v24
	ds_read_b128 v[24:27], v134 offset:27648
	s_waitcnt lgkmcnt(0)
	v_fmac_f32_e32 v77, v19, v27
	v_fmac_f32_e32 v77, v23, v26
	v_fmac_f32_e32 v77, v18, v25
	v_fmac_f32_e32 v77, v22, v24
	ds_read_b128 v[24:27], v134 offset:35840
	s_waitcnt lgkmcnt(0)
	v_fmac_f32_e32 v73, v19, v27
	v_fmac_f32_e32 v73, v23, v26
	v_fmac_f32_e32 v73, v18, v25
	v_fmac_f32_e32 v73, v22, v24
	ds_read_b128 v[24:27], v134 offset:44032
	s_waitcnt lgkmcnt(0)
	v_fmac_f32_e32 v69, v19, v27
	v_fmac_f32_e32 v69, v23, v26
	v_fmac_f32_e32 v69, v18, v25
	v_fmac_f32_e32 v69, v22, v24
	ds_read_b128 v[24:27], v134 offset:52224
	s_waitcnt lgkmcnt(0)
	v_fmac_f32_e32 v65, v19, v27
	v_fmac_f32_e32 v65, v23, v26
	v_fmac_f32_e32 v65, v18, v25
	v_fmac_f32_e32 v65, v22, v24
	ds_read_b128 v[24:27], v134 offset:60416
	s_waitcnt lgkmcnt(0)
	v_fmac_f32_e32 v61, v19, v27
	v_fmac_f32_e32 v61, v23, v26
	v_fmac_f32_e32 v61, v18, v25
	v_fmac_f32_e32 v61, v22, v24
	ds_read_b128 v[24:27], v162
	s_waitcnt lgkmcnt(0)
	v_fmac_f32_e32 v57, v19, v27
	v_fmac_f32_e32 v57, v23, v26
	v_fmac_f32_e32 v57, v18, v25
	v_fmac_f32_e32 v57, v22, v24
	ds_read_b128 v[24:27], v163
	s_waitcnt lgkmcnt(0)
	v_fmac_f32_e32 v53, v19, v27
	v_fmac_f32_e32 v53, v23, v26
	v_fmac_f32_e32 v53, v18, v25
	v_fmac_f32_e32 v53, v22, v24
	ds_read_b128 v[24:27], v164
	s_waitcnt lgkmcnt(0)
	v_fmac_f32_e32 v49, v19, v27
	v_fmac_f32_e32 v49, v23, v26
	v_fmac_f32_e32 v49, v18, v25
	v_fmac_f32_e32 v49, v22, v24
	ds_read_b128 v[24:27], v165
	s_waitcnt lgkmcnt(0)
	v_fmac_f32_e32 v45, v19, v27
	v_fmac_f32_e32 v45, v23, v26
	v_fmac_f32_e32 v45, v18, v25
	v_fmac_f32_e32 v45, v22, v24
	ds_read_b128 v[24:27], v166
	s_waitcnt lgkmcnt(0)
	v_fmac_f32_e32 v41, v19, v27
	v_fmac_f32_e32 v41, v23, v26
	v_fmac_f32_e32 v41, v18, v25
	v_fmac_f32_e32 v41, v22, v24
	ds_read_b128 v[24:27], v167
	s_waitcnt lgkmcnt(0)
	v_fmac_f32_e32 v37, v19, v27
	v_fmac_f32_e32 v37, v23, v26
	v_fmac_f32_e32 v37, v18, v25
	v_fmac_f32_e32 v37, v22, v24
	ds_read_b128 v[24:27], v168
	s_waitcnt lgkmcnt(0)
	v_fmac_f32_e32 v33, v19, v27
	v_fmac_f32_e32 v33, v23, v26
	v_fmac_f32_e32 v33, v18, v25
	v_fmac_f32_e32 v33, v22, v24
	ds_read_b128 v[24:27], v169
	s_waitcnt lgkmcnt(0)
	v_fmac_f32_e32 v30, v19, v27
	v_fmac_f32_e32 v30, v23, v26
	v_fmac_f32_e32 v30, v18, v25
	v_fmac_f32_e32 v30, v22, v24
	v_add_co_u32_e32 v18, vcc, s56, v118
	ds_read_b128 v[24:27], v170
	s_nop 0
	v_addc_co_u32_e32 v19, vcc, 0, v119, vcc
	v_add_co_u32_e32 v20, vcc, s56, v116
	flat_load_dwordx4 v[90:93], v[18:19]
	s_nop 0
	v_addc_co_u32_e32 v21, vcc, 0, v117, vcc
	flat_load_dwordx4 v[96:99], v[20:21]
	v_mov_b32_e32 v22, v14
	v_mov_b32_e32 v23, v16
	v_pk_mul_f32 v[22:23], v[22:23], v[114:115] op_sel_hi:[1,0]
	s_waitcnt lgkmcnt(0)
	v_mov_b32_e32 v28, v24
	v_mov_b32_e32 v29, v26
	v_pk_mul_f32 v[22:23], v[22:23], v[28:29]
	v_mov_b32_e32 v16, v15
	v_pk_mul_f32 v[14:15], v[16:17], v[114:115] op_sel_hi:[1,0]
	v_mov_b32_e32 v26, v25
	v_pk_mul_f32 v[14:15], v[14:15], v[26:27]
	s_waitcnt vmcnt(0)
	v_mov_b32_e32 v34, v90
	v_mov_b32_e32 v35, v92
	v_mov_b32_e32 v92, v91
	v_mov_b32_e32 v28, v96
	v_mov_b32_e32 v29, v98
	v_pk_add_f32 v[28:29], v[28:29], 1.0 op_sel_hi:[1,0]
	v_mov_b32_e32 v98, v97
	v_pk_fma_f32 v[22:23], v[22:23], v[28:29], v[34:35]
	v_pk_add_f32 v[16:17], v[98:99], 1.0 op_sel_hi:[1,0]
	s_nop 0
	v_pk_fma_f32 v[14:15], v[14:15], v[16:17], v[92:93]
	v_and_b32_sdwa v17, v22, v208 dst_sel:DWORD dst_unused:UNUSED_PAD src0_sel:WORD_1 src1_sel:DWORD
	v_add3_u32 v24, v22, v17, s57
	v_and_b32_sdwa v17, v15, v208 dst_sel:DWORD dst_unused:UNUSED_PAD src0_sel:WORD_1 src1_sel:DWORD
	v_and_b32_sdwa v25, v14, v208 dst_sel:DWORD dst_unused:UNUSED_PAD src0_sel:WORD_1 src1_sel:DWORD
	v_and_b32_sdwa v16, v23, v208 dst_sel:DWORD dst_unused:UNUSED_PAD src0_sel:WORD_1 src1_sel:DWORD
	v_add3_u32 v17, v15, v17, s57
	v_add3_u32 v25, v14, v25, s57
	v_add3_u32 v16, v23, v16, s57
	v_and_b32_e32 v17, 0xffff0000, v17
	v_and_b32_e32 v25, 0xffff0000, v25
	v_or_b32_sdwa v17, v17, v16 dst_sel:DWORD dst_unused:UNUSED_PAD src0_sel:DWORD src1_sel:WORD_1
	v_or_b32_sdwa v16, v25, v24 dst_sel:DWORD dst_unused:UNUSED_PAD src0_sel:DWORD src1_sel:WORD_1
	ds_read_b128 v[24:27], v134 offset:4096
	global_store_dwordx2 v[94:95], v[16:17], off offset:2048
	s_waitcnt lgkmcnt(0)
	v_fmac_f32_e32 v89, v15, v27
	v_fmac_f32_e32 v89, v23, v26
	v_fmac_f32_e32 v89, v14, v25
	v_fmac_f32_e32 v89, v22, v24
	ds_read_b128 v[24:27], v134 offset:12288
	s_waitcnt lgkmcnt(0)
	v_fmac_f32_e32 v85, v15, v27
	v_fmac_f32_e32 v85, v23, v26
	v_fmac_f32_e32 v85, v14, v25
	v_fmac_f32_e32 v85, v22, v24
	ds_read_b128 v[24:27], v134 offset:20480
	s_waitcnt lgkmcnt(0)
	v_fmac_f32_e32 v81, v15, v27
	v_fmac_f32_e32 v81, v23, v26
	v_fmac_f32_e32 v81, v14, v25
	v_fmac_f32_e32 v81, v22, v24
	ds_read_b128 v[24:27], v134 offset:28672
	s_waitcnt lgkmcnt(0)
	v_fmac_f32_e32 v77, v15, v27
	v_fmac_f32_e32 v77, v23, v26
	v_fmac_f32_e32 v77, v14, v25
	v_fmac_f32_e32 v77, v22, v24
	ds_read_b128 v[24:27], v134 offset:36864
	s_waitcnt lgkmcnt(0)
	v_fmac_f32_e32 v73, v15, v27
	v_fmac_f32_e32 v73, v23, v26
	v_fmac_f32_e32 v73, v14, v25
	v_fmac_f32_e32 v73, v22, v24
	ds_read_b128 v[24:27], v134 offset:45056
	s_waitcnt lgkmcnt(0)
	v_fmac_f32_e32 v69, v15, v27
	v_fmac_f32_e32 v69, v23, v26
	v_fmac_f32_e32 v69, v14, v25
	v_fmac_f32_e32 v69, v22, v24
	ds_read_b128 v[24:27], v134 offset:53248
	s_waitcnt lgkmcnt(0)
	v_fmac_f32_e32 v65, v15, v27
	v_fmac_f32_e32 v65, v23, v26
	v_fmac_f32_e32 v65, v14, v25
	v_fmac_f32_e32 v65, v22, v24
	ds_read_b128 v[24:27], v134 offset:61440
	s_waitcnt lgkmcnt(0)
	v_fmac_f32_e32 v61, v15, v27
	v_fmac_f32_e32 v61, v23, v26
	v_fmac_f32_e32 v61, v14, v25
	v_fmac_f32_e32 v61, v22, v24
	ds_read_b128 v[24:27], v171
	s_waitcnt lgkmcnt(0)
	v_fmac_f32_e32 v57, v15, v27
	v_fmac_f32_e32 v57, v23, v26
	v_fmac_f32_e32 v57, v14, v25
	v_fmac_f32_e32 v57, v22, v24
	ds_read_b128 v[24:27], v172
	s_waitcnt lgkmcnt(0)
	v_fmac_f32_e32 v53, v15, v27
	v_fmac_f32_e32 v53, v23, v26
	v_fmac_f32_e32 v53, v14, v25
	v_fmac_f32_e32 v53, v22, v24
	ds_read_b128 v[24:27], v173
	s_waitcnt lgkmcnt(0)
	v_fmac_f32_e32 v49, v15, v27
	v_fmac_f32_e32 v49, v23, v26
	v_fmac_f32_e32 v49, v14, v25
	v_fmac_f32_e32 v49, v22, v24
	ds_read_b128 v[24:27], v174
	s_waitcnt lgkmcnt(0)
	v_fmac_f32_e32 v45, v15, v27
	v_fmac_f32_e32 v45, v23, v26
	v_fmac_f32_e32 v45, v14, v25
	v_fmac_f32_e32 v45, v22, v24
	ds_read_b128 v[24:27], v175
	s_waitcnt lgkmcnt(0)
	v_fmac_f32_e32 v41, v15, v27
	v_fmac_f32_e32 v41, v23, v26
	v_fmac_f32_e32 v41, v14, v25
	v_fmac_f32_e32 v41, v22, v24
	ds_read_b128 v[24:27], v176
	s_waitcnt lgkmcnt(0)
	v_fmac_f32_e32 v37, v15, v27
	v_fmac_f32_e32 v37, v23, v26
	v_fmac_f32_e32 v37, v14, v25
	v_fmac_f32_e32 v37, v22, v24
	ds_read_b128 v[24:27], v177
	s_waitcnt lgkmcnt(0)
	v_fmac_f32_e32 v33, v15, v27
	v_fmac_f32_e32 v33, v23, v26
	v_fmac_f32_e32 v33, v14, v25
	v_fmac_f32_e32 v33, v22, v24
	ds_read_b128 v[24:27], v178
	s_waitcnt lgkmcnt(0)
	v_fmac_f32_e32 v30, v15, v27
	v_fmac_f32_e32 v30, v23, v26
	v_fmac_f32_e32 v30, v14, v25
	v_fmac_f32_e32 v30, v22, v24
	ds_read_b128 v[22:25], v179
	flat_load_dwordx4 v[26:29], v[18:19] offset:1024
	flat_load_dwordx4 v[90:93], v[20:21] offset:1024
	v_mov_b32_e32 v15, v12
	v_mov_b32_e32 v12, v11
	v_mov_b32_e32 v14, v10
	s_waitcnt lgkmcnt(0)
	v_mov_b32_e32 v17, v24
	v_pk_mul_f32 v[10:11], v[12:13], v[114:115] op_sel_hi:[1,0]
	v_mov_b32_e32 v24, v23
	v_mov_b32_e32 v16, v22
	v_pk_mul_f32 v[10:11], v[10:11], v[24:25]
	ds_read_b128 v[22:25], v134 offset:5120
	v_pk_mul_f32 v[14:15], v[14:15], v[114:115] op_sel_hi:[1,0]
	s_waitcnt vmcnt(0)
	v_mov_b32_e32 v35, v28
	v_pk_mul_f32 v[14:15], v[14:15], v[16:17]
	v_mov_b32_e32 v17, v92
	v_mov_b32_e32 v92, v91
	v_mov_b32_e32 v16, v90
	v_pk_add_f32 v[12:13], v[92:93], 1.0 op_sel_hi:[1,0]
	v_mov_b32_e32 v28, v27
	v_pk_add_f32 v[16:17], v[16:17], 1.0 op_sel_hi:[1,0]
	v_mov_b32_e32 v34, v26
	v_pk_fma_f32 v[10:11], v[10:11], v[12:13], v[28:29]
	v_pk_fma_f32 v[14:15], v[14:15], v[16:17], v[34:35]
	s_waitcnt lgkmcnt(0)
	v_fmac_f32_e32 v89, v11, v25
	v_fmac_f32_e32 v89, v15, v24
	v_fmac_f32_e32 v89, v10, v23
	v_fmac_f32_e32 v89, v14, v22
	ds_read_b128 v[22:25], v134 offset:13312
	v_and_b32_sdwa v13, v14, v208 dst_sel:DWORD dst_unused:UNUSED_PAD src0_sel:WORD_1 src1_sel:DWORD
	v_add3_u32 v16, v14, v13, s57
	v_and_b32_sdwa v13, v11, v208 dst_sel:DWORD dst_unused:UNUSED_PAD src0_sel:WORD_1 src1_sel:DWORD
	v_and_b32_sdwa v17, v10, v208 dst_sel:DWORD dst_unused:UNUSED_PAD src0_sel:WORD_1 src1_sel:DWORD
	s_waitcnt lgkmcnt(0)
	v_fmac_f32_e32 v85, v11, v25
	v_fmac_f32_e32 v85, v15, v24
	v_fmac_f32_e32 v85, v10, v23
	v_fmac_f32_e32 v85, v14, v22
	ds_read_b128 v[22:25], v134 offset:21504
	v_and_b32_sdwa v12, v15, v208 dst_sel:DWORD dst_unused:UNUSED_PAD src0_sel:WORD_1 src1_sel:DWORD
	v_add3_u32 v13, v11, v13, s57
	v_add3_u32 v17, v10, v17, s57
	v_add3_u32 v12, v15, v12, s57
	s_waitcnt lgkmcnt(0)
	v_fmac_f32_e32 v81, v11, v25
	v_fmac_f32_e32 v81, v15, v24
	v_fmac_f32_e32 v81, v10, v23
	v_fmac_f32_e32 v81, v14, v22
	ds_read_b128 v[22:25], v134 offset:29696
	v_and_b32_e32 v13, 0xffff0000, v13
	v_and_b32_e32 v17, 0xffff0000, v17
	v_or_b32_sdwa v13, v13, v12 dst_sel:DWORD dst_unused:UNUSED_PAD src0_sel:DWORD src1_sel:WORD_1
	v_or_b32_sdwa v12, v17, v16 dst_sel:DWORD dst_unused:UNUSED_PAD src0_sel:DWORD src1_sel:WORD_1
	s_waitcnt lgkmcnt(0)
	v_fmac_f32_e32 v77, v11, v25
	v_fmac_f32_e32 v77, v15, v24
	v_fmac_f32_e32 v77, v10, v23
	v_fmac_f32_e32 v77, v14, v22
	ds_read_b128 v[22:25], v134 offset:37888
	global_store_dwordx2 v[94:95], v[12:13], off offset:2560
	s_waitcnt lgkmcnt(0)
	v_fmac_f32_e32 v73, v11, v25
	v_fmac_f32_e32 v73, v15, v24
	v_fmac_f32_e32 v73, v10, v23
	v_fmac_f32_e32 v73, v14, v22
	ds_read_b128 v[22:25], v134 offset:46080
	s_waitcnt lgkmcnt(0)
	v_fmac_f32_e32 v69, v11, v25
	v_fmac_f32_e32 v69, v15, v24
	v_fmac_f32_e32 v69, v10, v23
	v_fmac_f32_e32 v69, v14, v22
	ds_read_b128 v[22:25], v134 offset:54272
	s_waitcnt lgkmcnt(0)
	v_fmac_f32_e32 v65, v11, v25
	v_fmac_f32_e32 v65, v15, v24
	v_fmac_f32_e32 v65, v10, v23
	v_fmac_f32_e32 v65, v14, v22
	ds_read_b128 v[22:25], v134 offset:62464
	s_waitcnt lgkmcnt(0)
	v_fmac_f32_e32 v61, v11, v25
	v_fmac_f32_e32 v61, v15, v24
	v_fmac_f32_e32 v61, v10, v23
	v_fmac_f32_e32 v61, v14, v22
	ds_read_b128 v[22:25], v180
	s_waitcnt lgkmcnt(0)
	v_fmac_f32_e32 v57, v11, v25
	v_fmac_f32_e32 v57, v15, v24
	v_fmac_f32_e32 v57, v10, v23
	v_fmac_f32_e32 v57, v14, v22
	ds_read_b128 v[22:25], v181
	s_waitcnt lgkmcnt(0)
	v_fmac_f32_e32 v53, v11, v25
	v_fmac_f32_e32 v53, v15, v24
	v_fmac_f32_e32 v53, v10, v23
	v_fmac_f32_e32 v53, v14, v22
	ds_read_b128 v[22:25], v182
	s_waitcnt lgkmcnt(0)
	v_fmac_f32_e32 v49, v11, v25
	v_fmac_f32_e32 v49, v15, v24
	v_fmac_f32_e32 v49, v10, v23
	v_fmac_f32_e32 v49, v14, v22
	ds_read_b128 v[22:25], v183
	s_waitcnt lgkmcnt(0)
	v_fmac_f32_e32 v45, v11, v25
	v_fmac_f32_e32 v45, v15, v24
	v_fmac_f32_e32 v45, v10, v23
	v_fmac_f32_e32 v45, v14, v22
	ds_read_b128 v[22:25], v184
	s_waitcnt lgkmcnt(0)
	v_fmac_f32_e32 v41, v11, v25
	v_fmac_f32_e32 v41, v15, v24
	v_fmac_f32_e32 v41, v10, v23
	v_fmac_f32_e32 v41, v14, v22
	ds_read_b128 v[22:25], v185
	s_waitcnt lgkmcnt(0)
	v_fmac_f32_e32 v37, v11, v25
	v_fmac_f32_e32 v37, v15, v24
	v_fmac_f32_e32 v37, v10, v23
	v_fmac_f32_e32 v37, v14, v22
	ds_read_b128 v[22:25], v186
	s_waitcnt lgkmcnt(0)
	v_fmac_f32_e32 v33, v11, v25
	v_fmac_f32_e32 v33, v15, v24
	v_fmac_f32_e32 v33, v10, v23
	v_fmac_f32_e32 v33, v14, v22
	ds_read_b128 v[22:25], v187
	s_waitcnt lgkmcnt(0)
	v_fmac_f32_e32 v30, v11, v25
	v_fmac_f32_e32 v30, v15, v24
	v_fmac_f32_e32 v30, v10, v23
	v_fmac_f32_e32 v30, v14, v22
	ds_read_b128 v[12:15], v188
	flat_load_dwordx4 v[22:25], v[18:19] offset:2048
	flat_load_dwordx4 v[26:29], v[20:21] offset:2048
	v_mov_b32_e32 v10, v6
	v_mov_b32_e32 v11, v8
	v_pk_mul_f32 v[10:11], v[10:11], v[114:115] op_sel_hi:[1,0]
	s_waitcnt lgkmcnt(0)
	v_mov_b32_e32 v16, v12
	v_mov_b32_e32 v17, v14
	v_pk_mul_f32 v[10:11], v[10:11], v[16:17]
	v_mov_b32_e32 v8, v7
	v_pk_mul_f32 v[6:7], v[8:9], v[114:115] op_sel_hi:[1,0]
	v_mov_b32_e32 v14, v13
	v_pk_mul_f32 v[6:7], v[6:7], v[14:15]
	s_waitcnt vmcnt(0)
	v_mov_b32_e32 v34, v22
	v_mov_b32_e32 v16, v26
	v_mov_b32_e32 v17, v28
	v_pk_add_f32 v[16:17], v[16:17], 1.0 op_sel_hi:[1,0]
	v_mov_b32_e32 v35, v24
	v_mov_b32_e32 v28, v27
	v_pk_fma_f32 v[10:11], v[10:11], v[16:17], v[34:35]
	v_pk_add_f32 v[8:9], v[28:29], 1.0 op_sel_hi:[1,0]
	v_mov_b32_e32 v24, v23
	v_pk_fma_f32 v[6:7], v[6:7], v[8:9], v[24:25]
	v_and_b32_sdwa v9, v10, v208 dst_sel:DWORD dst_unused:UNUSED_PAD src0_sel:WORD_1 src1_sel:DWORD
	v_add3_u32 v12, v10, v9, s57
	v_and_b32_sdwa v9, v7, v208 dst_sel:DWORD dst_unused:UNUSED_PAD src0_sel:WORD_1 src1_sel:DWORD
	v_and_b32_sdwa v13, v6, v208 dst_sel:DWORD dst_unused:UNUSED_PAD src0_sel:WORD_1 src1_sel:DWORD
	v_and_b32_sdwa v8, v11, v208 dst_sel:DWORD dst_unused:UNUSED_PAD src0_sel:WORD_1 src1_sel:DWORD
	v_add3_u32 v9, v7, v9, s57
	v_add3_u32 v13, v6, v13, s57
	v_add3_u32 v8, v11, v8, s57
	v_and_b32_e32 v9, 0xffff0000, v9
	v_and_b32_e32 v13, 0xffff0000, v13
	v_or_b32_sdwa v9, v9, v8 dst_sel:DWORD dst_unused:UNUSED_PAD src0_sel:DWORD src1_sel:WORD_1
	v_or_b32_sdwa v8, v13, v12 dst_sel:DWORD dst_unused:UNUSED_PAD src0_sel:DWORD src1_sel:WORD_1
	ds_read_b128 v[12:15], v134 offset:6144
	global_store_dwordx2 v[94:95], v[8:9], off offset:3072
	s_waitcnt lgkmcnt(0)
	v_fmac_f32_e32 v89, v7, v15
	v_fmac_f32_e32 v89, v11, v14
	v_fmac_f32_e32 v89, v6, v13
	v_fmac_f32_e32 v89, v10, v12
	ds_read_b128 v[12:15], v134 offset:14336
	s_waitcnt lgkmcnt(0)
	v_fmac_f32_e32 v85, v7, v15
	v_fmac_f32_e32 v85, v11, v14
	v_fmac_f32_e32 v85, v6, v13
	v_fmac_f32_e32 v85, v10, v12
	ds_read_b128 v[12:15], v134 offset:22528
	s_waitcnt lgkmcnt(0)
	v_fmac_f32_e32 v81, v7, v15
	v_fmac_f32_e32 v81, v11, v14
	v_fmac_f32_e32 v81, v6, v13
	v_fmac_f32_e32 v81, v10, v12
	ds_read_b128 v[12:15], v134 offset:30720
	s_waitcnt lgkmcnt(0)
	v_fmac_f32_e32 v77, v7, v15
	v_fmac_f32_e32 v77, v11, v14
	v_fmac_f32_e32 v77, v6, v13
	v_fmac_f32_e32 v77, v10, v12
	ds_read_b128 v[12:15], v134 offset:38912
	s_waitcnt lgkmcnt(0)
	v_fmac_f32_e32 v73, v7, v15
	v_fmac_f32_e32 v73, v11, v14
	v_fmac_f32_e32 v73, v6, v13
	v_fmac_f32_e32 v73, v10, v12
	ds_read_b128 v[12:15], v134 offset:47104
	s_waitcnt lgkmcnt(0)
	v_fmac_f32_e32 v69, v7, v15
	v_fmac_f32_e32 v69, v11, v14
	v_fmac_f32_e32 v69, v6, v13
	v_fmac_f32_e32 v69, v10, v12
	ds_read_b128 v[12:15], v134 offset:55296
	s_waitcnt lgkmcnt(0)
	v_fmac_f32_e32 v65, v7, v15
	v_fmac_f32_e32 v65, v11, v14
	v_fmac_f32_e32 v65, v6, v13
	v_fmac_f32_e32 v65, v10, v12
	ds_read_b128 v[12:15], v134 offset:63488
	s_waitcnt lgkmcnt(0)
	v_fmac_f32_e32 v61, v7, v15
	v_fmac_f32_e32 v61, v11, v14
	v_fmac_f32_e32 v61, v6, v13
	v_fmac_f32_e32 v61, v10, v12
	ds_read_b128 v[12:15], v189
	s_waitcnt lgkmcnt(0)
	v_fmac_f32_e32 v57, v7, v15
	v_fmac_f32_e32 v57, v11, v14
	v_fmac_f32_e32 v57, v6, v13
	v_fmac_f32_e32 v57, v10, v12
	ds_read_b128 v[12:15], v191
	s_waitcnt lgkmcnt(0)
	v_fmac_f32_e32 v53, v7, v15
	v_fmac_f32_e32 v53, v11, v14
	v_fmac_f32_e32 v53, v6, v13
	v_fmac_f32_e32 v53, v10, v12
	ds_read_b128 v[12:15], v192
	s_waitcnt lgkmcnt(0)
	v_fmac_f32_e32 v49, v7, v15
	v_fmac_f32_e32 v49, v11, v14
	v_fmac_f32_e32 v49, v6, v13
	v_fmac_f32_e32 v49, v10, v12
	ds_read_b128 v[12:15], v193
	s_waitcnt lgkmcnt(0)
	v_fmac_f32_e32 v45, v7, v15
	v_fmac_f32_e32 v45, v11, v14
	v_fmac_f32_e32 v45, v6, v13
	v_fmac_f32_e32 v45, v10, v12
	ds_read_b128 v[12:15], v194
	s_waitcnt lgkmcnt(0)
	v_fmac_f32_e32 v41, v7, v15
	v_fmac_f32_e32 v41, v11, v14
	v_fmac_f32_e32 v41, v6, v13
	v_fmac_f32_e32 v41, v10, v12
	ds_read_b128 v[12:15], v195
	s_waitcnt lgkmcnt(0)
	v_fmac_f32_e32 v37, v7, v15
	v_fmac_f32_e32 v37, v11, v14
	v_fmac_f32_e32 v37, v6, v13
	v_fmac_f32_e32 v37, v10, v12
	ds_read_b128 v[12:15], v196
	s_waitcnt lgkmcnt(0)
	v_fmac_f32_e32 v33, v7, v15
	v_fmac_f32_e32 v33, v11, v14
	v_fmac_f32_e32 v33, v6, v13
	v_fmac_f32_e32 v33, v10, v12
	ds_read_b128 v[12:15], v197
	s_waitcnt lgkmcnt(0)
	v_fmac_f32_e32 v30, v7, v15
	v_fmac_f32_e32 v30, v11, v14
	v_fmac_f32_e32 v30, v6, v13
	v_fmac_f32_e32 v30, v10, v12
	ds_read_b128 v[8:11], v198
	flat_load_dwordx4 v[12:15], v[18:19] offset:3072
	s_nop 0
	flat_load_dwordx4 v[16:19], v[20:21] offset:3072
	v_mov_b32_e32 v6, v2
	v_mov_b32_e32 v7, v4
	v_pk_mul_f32 v[6:7], v[6:7], v[114:115] op_sel_hi:[1,0]
	s_waitcnt lgkmcnt(0)
	v_mov_b32_e32 v20, v8
	v_mov_b32_e32 v21, v10
	v_pk_mul_f32 v[6:7], v[6:7], v[20:21]
	v_mov_b32_e32 v4, v3
	v_pk_mul_f32 v[2:3], v[4:5], v[114:115] op_sel_hi:[1,0]
	v_mov_b32_e32 v10, v9
	v_pk_mul_f32 v[2:3], v[2:3], v[10:11]
	s_waitcnt vmcnt(0)
	v_mov_b32_e32 v22, v12
	v_mov_b32_e32 v20, v16
	v_mov_b32_e32 v21, v18
	v_pk_add_f32 v[20:21], v[20:21], 1.0 op_sel_hi:[1,0]
	v_mov_b32_e32 v23, v14
	v_mov_b32_e32 v18, v17
	v_pk_fma_f32 v[6:7], v[6:7], v[20:21], v[22:23]
	v_pk_add_f32 v[4:5], v[18:19], 1.0 op_sel_hi:[1,0]
	v_mov_b32_e32 v14, v13
	v_pk_fma_f32 v[2:3], v[2:3], v[4:5], v[14:15]
	v_and_b32_sdwa v5, v6, v208 dst_sel:DWORD dst_unused:UNUSED_PAD src0_sel:WORD_1 src1_sel:DWORD
	v_add3_u32 v8, v6, v5, s57
	v_and_b32_sdwa v5, v3, v208 dst_sel:DWORD dst_unused:UNUSED_PAD src0_sel:WORD_1 src1_sel:DWORD
	v_and_b32_sdwa v9, v2, v208 dst_sel:DWORD dst_unused:UNUSED_PAD src0_sel:WORD_1 src1_sel:DWORD
	v_and_b32_sdwa v4, v7, v208 dst_sel:DWORD dst_unused:UNUSED_PAD src0_sel:WORD_1 src1_sel:DWORD
	v_add3_u32 v5, v3, v5, s57
	v_add3_u32 v9, v2, v9, s57
	v_add3_u32 v4, v7, v4, s57
	v_and_b32_e32 v5, 0xffff0000, v5
	v_and_b32_e32 v9, 0xffff0000, v9
	v_or_b32_sdwa v5, v5, v4 dst_sel:DWORD dst_unused:UNUSED_PAD src0_sel:DWORD src1_sel:WORD_1
	v_or_b32_sdwa v4, v9, v8 dst_sel:DWORD dst_unused:UNUSED_PAD src0_sel:DWORD src1_sel:WORD_1
	ds_read_b128 v[8:11], v134 offset:7168
	global_store_dwordx2 v[94:95], v[4:5], off offset:3584
	s_waitcnt lgkmcnt(0)
	v_fmac_f32_e32 v89, v3, v11
	v_fmac_f32_e32 v89, v7, v10
	v_fmac_f32_e32 v89, v2, v9
	v_fmac_f32_e32 v89, v6, v8
	ds_read_b128 v[8:11], v134 offset:15360
	s_waitcnt lgkmcnt(0)
	v_fmac_f32_e32 v85, v3, v11
	v_fmac_f32_e32 v85, v7, v10
	v_fmac_f32_e32 v85, v2, v9
	v_fmac_f32_e32 v85, v6, v8
	ds_read_b128 v[8:11], v134 offset:23552
	s_waitcnt lgkmcnt(0)
	v_fmac_f32_e32 v81, v3, v11
	v_fmac_f32_e32 v81, v7, v10
	v_fmac_f32_e32 v81, v2, v9
	v_fmac_f32_e32 v81, v6, v8
	ds_read_b128 v[8:11], v134 offset:31744
	s_waitcnt lgkmcnt(0)
	v_fmac_f32_e32 v77, v3, v11
	v_fmac_f32_e32 v77, v7, v10
	v_fmac_f32_e32 v77, v2, v9
	v_fmac_f32_e32 v77, v6, v8
	ds_read_b128 v[8:11], v134 offset:39936
	s_waitcnt lgkmcnt(0)
	v_fmac_f32_e32 v73, v3, v11
	v_fmac_f32_e32 v73, v7, v10
	v_fmac_f32_e32 v73, v2, v9
	v_fmac_f32_e32 v73, v6, v8
	ds_read_b128 v[8:11], v134 offset:48128
	s_waitcnt lgkmcnt(0)
	v_fmac_f32_e32 v69, v3, v11
	v_fmac_f32_e32 v69, v7, v10
	v_fmac_f32_e32 v69, v2, v9
	v_fmac_f32_e32 v69, v6, v8
	ds_read_b128 v[8:11], v134 offset:56320
	s_waitcnt lgkmcnt(0)
	v_fmac_f32_e32 v65, v3, v11
	v_fmac_f32_e32 v65, v7, v10
	v_fmac_f32_e32 v65, v2, v9
	v_fmac_f32_e32 v65, v6, v8
	ds_read_b128 v[8:11], v134 offset:64512
	s_waitcnt lgkmcnt(0)
	v_fmac_f32_e32 v61, v3, v11
	v_fmac_f32_e32 v61, v7, v10
	v_fmac_f32_e32 v61, v2, v9
	v_fmac_f32_e32 v61, v6, v8
	ds_read_b128 v[8:11], v199
	s_waitcnt lgkmcnt(0)
	v_fmac_f32_e32 v57, v3, v11
	v_fmac_f32_e32 v57, v7, v10
	v_fmac_f32_e32 v57, v2, v9
	v_fmac_f32_e32 v57, v6, v8
	ds_read_b128 v[8:11], v200
	s_waitcnt lgkmcnt(0)
	v_fmac_f32_e32 v53, v3, v11
	v_fmac_f32_e32 v53, v7, v10
	v_fmac_f32_e32 v53, v2, v9
	v_fmac_f32_e32 v53, v6, v8
	ds_read_b128 v[8:11], v201
	s_waitcnt lgkmcnt(0)
	v_fmac_f32_e32 v49, v3, v11
	v_fmac_f32_e32 v49, v7, v10
	v_fmac_f32_e32 v49, v2, v9
	v_fmac_f32_e32 v49, v6, v8
	ds_read_b128 v[8:11], v202
	s_waitcnt lgkmcnt(0)
	v_fmac_f32_e32 v45, v3, v11
	v_fmac_f32_e32 v45, v7, v10
	v_fmac_f32_e32 v45, v2, v9
	v_fmac_f32_e32 v45, v6, v8
	ds_read_b128 v[8:11], v203
	s_waitcnt lgkmcnt(0)
	v_fmac_f32_e32 v41, v3, v11
	v_fmac_f32_e32 v41, v7, v10
	v_fmac_f32_e32 v41, v2, v9
	v_fmac_f32_e32 v41, v6, v8
	ds_read_b128 v[8:11], v204
	s_waitcnt lgkmcnt(0)
	v_fmac_f32_e32 v37, v3, v11
	v_fmac_f32_e32 v37, v7, v10
	v_fmac_f32_e32 v37, v2, v9
	v_fmac_f32_e32 v37, v6, v8
	ds_read_b128 v[8:11], v205
	s_waitcnt lgkmcnt(0)
	v_fmac_f32_e32 v33, v3, v11
	v_fmac_f32_e32 v33, v7, v10
	v_fmac_f32_e32 v33, v2, v9
	v_fmac_f32_e32 v33, v6, v8
	ds_read_b128 v[8:11], v206
	s_waitcnt lgkmcnt(0)
	v_fmac_f32_e32 v30, v3, v11
	v_fmac_f32_e32 v30, v7, v10
	v_fmac_f32_e32 v30, v2, v9
	v_fmac_f32_e32 v30, v6, v8
	ds_bpermute_b32 v6, v1, v81
	ds_bpermute_b32 v7, v1, v77
	ds_bpermute_b32 v22, v1, v49
	ds_bpermute_b32 v10, v1, v73
	ds_bpermute_b32 v24, v1, v41
	s_waitcnt lgkmcnt(4)
	v_add_f32_e32 v6, v81, v6
	ds_bpermute_b32 v8, v128, v6
	s_waitcnt lgkmcnt(4)
	v_add_f32_e32 v7, v77, v7
	ds_bpermute_b32 v9, v128, v7
	s_waitcnt lgkmcnt(4)
	v_add_f32_e32 v22, v49, v22
	ds_bpermute_b32 v23, v128, v22
	s_waitcnt lgkmcnt(2)
	v_add_f32_e32 v6, v6, v8
	ds_bpermute_b32 v8, v129, v6
	s_waitcnt lgkmcnt(2)
	v_add_f32_e32 v7, v7, v9
	ds_bpermute_b32 v9, v129, v7
	s_waitcnt lgkmcnt(2)
	v_add_f32_e32 v22, v22, v23
	ds_bpermute_b32 v23, v129, v22
	s_waitcnt lgkmcnt(2)
	v_add_f32_e32 v6, v6, v8
	ds_bpermute_b32 v8, v130, v6
	s_waitcnt lgkmcnt(2)
	v_add_f32_e32 v7, v7, v9
	ds_bpermute_b32 v9, v130, v7
	v_add_f32_e32 v10, v73, v10
	s_waitcnt lgkmcnt(2)
	v_add_f32_e32 v22, v22, v23
	s_waitcnt lgkmcnt(1)
	v_add_f32_e32 v6, v6, v8
	ds_bpermute_b32 v8, v131, v6
	s_waitcnt lgkmcnt(1)
	v_add_f32_e32 v9, v7, v9
	ds_bpermute_b32 v12, v131, v9
	v_add_f32_e32 v23, v41, v24
	ds_bpermute_b32 v11, v128, v10
	s_waitcnt lgkmcnt(2)
	v_add_f32_e32 v6, v6, v8
	ds_bpermute_b32 v8, v1, v69
	ds_bpermute_b32 v24, v128, v23
	ds_bpermute_b32 v27, v130, v22
	s_waitcnt lgkmcnt(3)
	v_add_f32_e32 v10, v10, v11
	ds_bpermute_b32 v11, v129, v10
	s_waitcnt lgkmcnt(3)
	v_add_f32_e32 v13, v69, v8
	ds_bpermute_b32 v14, v128, v13
	v_add_f32_e32 v8, v9, v12
	s_waitcnt lgkmcnt(3)
	v_add_f32_e32 v23, v23, v24
	ds_bpermute_b32 v24, v129, v23
	s_waitcnt lgkmcnt(2)
	v_add_f32_e32 v10, v10, v11
	s_waitcnt lgkmcnt(1)
	v_add_f32_e32 v12, v13, v14
	ds_bpermute_b32 v14, v1, v65
	v_add_f32_e32 v22, v22, v27
	s_waitcnt lgkmcnt(1)
	v_add_f32_e32 v23, v23, v24
	ds_bpermute_b32 v11, v130, v10
	ds_bpermute_b32 v27, v131, v22
	s_waitcnt lgkmcnt(2)
	v_add_f32_e32 v14, v65, v14
	ds_bpermute_b32 v15, v128, v14
	ds_bpermute_b32 v24, v130, v23
	s_waitcnt lgkmcnt(3)
	v_add_f32_e32 v10, v10, v11
	s_waitcnt lgkmcnt(2)
	v_add_f32_e32 v22, v22, v27
	ds_bpermute_b32 v11, v131, v10
	s_waitcnt lgkmcnt(2)
	v_add_f32_e32 v14, v14, v15
	ds_bpermute_b32 v15, v129, v14
	s_waitcnt lgkmcnt(2)
	v_add_f32_e32 v27, v23, v24
	ds_bpermute_b32 v28, v131, v27
	ds_bpermute_b32 v2, v1, v89
	ds_bpermute_b32 v3, v1, v85
	s_waitcnt lgkmcnt(3)
	v_add_f32_e32 v14, v14, v15
	ds_bpermute_b32 v15, v130, v14
	v_add_f32_e32 v10, v10, v11
	ds_bpermute_b32 v11, v1, v61
	ds_bpermute_b32 v18, v1, v57
	ds_bpermute_b32 v29, v1, v37
	s_waitcnt lgkmcnt(3)
	v_add_f32_e32 v14, v14, v15
	ds_bpermute_b32 v15, v131, v14
	ds_bpermute_b32 v31, v1, v30
	v_add_f32_e32 v2, v89, v2
	v_add_f32_e32 v3, v85, v3
	s_waitcnt lgkmcnt(4)
	v_add_f32_e32 v16, v61, v11
	s_waitcnt lgkmcnt(1)
	v_add_f32_e32 v14, v14, v15
	ds_bpermute_b32 v15, v1, v53
	v_add_f32_e32 v18, v57, v18
	v_add_f32_e32 v29, v37, v29
	s_waitcnt lgkmcnt(1)
	v_add_f32_e32 v30, v30, v31
	ds_bpermute_b32 v4, v128, v2
	s_waitcnt lgkmcnt(1)
	v_add_f32_e32 v20, v53, v15
	ds_bpermute_b32 v21, v128, v20
	ds_bpermute_b32 v5, v128, v3
	ds_bpermute_b32 v17, v128, v16
	ds_bpermute_b32 v19, v128, v18
	ds_bpermute_b32 v32, v128, v29
	s_waitcnt lgkmcnt(4)
	v_add_f32_e32 v20, v20, v21
	ds_bpermute_b32 v21, v129, v20
	ds_bpermute_b32 v31, v128, v30
	v_add_f32_e32 v2, v2, v4
	s_waitcnt lgkmcnt(5)
	v_add_f32_e32 v3, v3, v5
	s_waitcnt lgkmcnt(4)
	v_add_f32_e32 v16, v16, v17
	s_waitcnt lgkmcnt(1)
	v_add_f32_e32 v20, v20, v21
	ds_bpermute_b32 v21, v130, v20
	v_add_f32_e32 v18, v18, v19
	v_add_f32_e32 v29, v29, v32
	s_waitcnt lgkmcnt(1)
	v_add_f32_e32 v30, v30, v31
	ds_bpermute_b32 v4, v129, v2
	s_waitcnt lgkmcnt(1)
	v_add_f32_e32 v20, v20, v21
	ds_bpermute_b32 v21, v1, v45
	ds_bpermute_b32 v25, v131, v20
	ds_bpermute_b32 v5, v129, v3
	ds_bpermute_b32 v13, v129, v12
	ds_bpermute_b32 v17, v129, v16
	s_waitcnt lgkmcnt(4)
	v_add_f32_e32 v21, v45, v21
	ds_bpermute_b32 v26, v128, v21
	s_waitcnt lgkmcnt(4)
	v_add_f32_e32 v20, v20, v25
	ds_bpermute_b32 v19, v129, v18
	ds_bpermute_b32 v32, v129, v29
	ds_bpermute_b32 v31, v129, v30
	s_waitcnt lgkmcnt(3)
	v_add_f32_e32 v21, v21, v26
	ds_bpermute_b32 v26, v129, v21
	v_add_f32_e32 v2, v2, v4
	v_add_f32_e32 v3, v3, v5
	v_add_f32_e32 v12, v12, v13
	v_add_f32_e32 v16, v16, v17
	s_waitcnt lgkmcnt(0)
	v_add_f32_e32 v25, v21, v26
	ds_bpermute_b32 v26, v130, v25
	v_add_f32_e32 v18, v18, v19
	v_add_f32_e32 v29, v29, v32
	v_add_f32_e32 v30, v30, v31
	ds_bpermute_b32 v4, v130, v2
	s_waitcnt lgkmcnt(1)
	v_add_f32_e32 v25, v25, v26
	ds_bpermute_b32 v26, v131, v25
	ds_bpermute_b32 v5, v130, v3
	ds_bpermute_b32 v13, v130, v12
	ds_bpermute_b32 v17, v130, v16
	ds_bpermute_b32 v19, v130, v18
	s_waitcnt lgkmcnt(4)
	v_add_f32_e32 v24, v25, v26
	v_add_f32_e32 v26, v27, v28
	ds_bpermute_b32 v28, v1, v33
	ds_bpermute_b32 v32, v130, v29
	ds_bpermute_b32 v31, v130, v30
	v_add_f32_e32 v2, v2, v4
	s_waitcnt lgkmcnt(6)
	v_add_f32_e32 v3, v3, v5
	s_waitcnt lgkmcnt(2)
	v_add_f32_e32 v28, v33, v28
	ds_bpermute_b32 v33, v128, v28
	v_add_f32_e32 v12, v12, v13
	v_add_f32_e32 v16, v16, v17
	v_add_f32_e32 v18, v18, v19
	s_waitcnt lgkmcnt(2)
	v_add_f32_e32 v29, v29, v32
	s_waitcnt lgkmcnt(0)
	v_add_f32_e32 v28, v28, v33
	ds_bpermute_b32 v33, v129, v28
	v_add_f32_e32 v35, v30, v31
	ds_bpermute_b32 v4, v131, v2
	ds_bpermute_b32 v5, v131, v3
	ds_bpermute_b32 v13, v131, v12
	s_waitcnt lgkmcnt(3)
	v_add_f32_e32 v28, v28, v33
	ds_bpermute_b32 v33, v130, v28
	ds_bpermute_b32 v17, v131, v16
	ds_bpermute_b32 v19, v131, v18
	ds_bpermute_b32 v32, v131, v29
	ds_bpermute_b32 v36, v131, v35
	s_waitcnt lgkmcnt(4)
	v_add_f32_e32 v33, v28, v33
	ds_bpermute_b32 v34, v131, v33
	v_add_f32_e32 v2, v2, v4
	v_add_f32_e32 v3, v3, v5
	v_add_f32_e32 v12, v12, v13
	s_waitcnt lgkmcnt(4)
	v_add_f32_e32 v16, v16, v17
	s_waitcnt lgkmcnt(3)
	v_add_f32_e32 v18, v18, v19
	s_waitcnt lgkmcnt(2)
	v_add_f32_e32 v28, v29, v32
	s_waitcnt lgkmcnt(0)
	v_add_f32_e32 v29, v33, v34
	v_add_f32_e32 v32, v35, v36
	ds_bpermute_b32 v4, v132, v2
	ds_bpermute_b32 v5, v132, v3
	ds_bpermute_b32 v7, v132, v6
	ds_bpermute_b32 v9, v132, v8
	ds_bpermute_b32 v11, v132, v10
	ds_bpermute_b32 v13, v132, v12
	ds_bpermute_b32 v15, v132, v14
	ds_bpermute_b32 v17, v132, v16
	ds_bpermute_b32 v19, v132, v18
	ds_bpermute_b32 v21, v132, v20
	ds_bpermute_b32 v23, v132, v22
	ds_bpermute_b32 v25, v132, v24
	ds_bpermute_b32 v27, v132, v26
	ds_bpermute_b32 v30, v132, v28
	ds_bpermute_b32 v31, v132, v29
	ds_bpermute_b32 v33, v132, v32
	s_and_saveexec_b64 s[52:53], s[2:3]
	s_cbranch_execz .LBB0_1364
	s_waitcnt lgkmcnt(14)
	v_add_f32_e32 v2, v2, v4
	v_add_f32_e32 v3, v3, v5
	s_mov_b32 s61, 0xff61b1e6
	v_max3_f32 v4, v2, s61, v3
	s_waitcnt lgkmcnt(13)
	v_add_f32_e32 v5, v6, v7
	s_waitcnt lgkmcnt(12)
	v_add_f32_e32 v6, v8, v9
	v_max3_f32 v4, v4, v5, v6
	s_waitcnt lgkmcnt(11)
	v_add_f32_e32 v7, v10, v11
	s_waitcnt lgkmcnt(10)
	v_add_f32_e32 v8, v12, v13
	v_max3_f32 v4, v4, v7, v8
	s_waitcnt lgkmcnt(9)
	v_add_f32_e32 v11, v14, v15
	s_waitcnt lgkmcnt(8)
	v_add_f32_e32 v15, v16, v17
	v_max3_f32 v4, v4, v11, v15
	s_waitcnt lgkmcnt(7)
	v_add_f32_e32 v16, v18, v19
	s_waitcnt lgkmcnt(6)
	v_add_f32_e32 v17, v20, v21
	v_max3_f32 v4, v4, v16, v17
	s_waitcnt lgkmcnt(5)
	v_add_f32_e32 v18, v22, v23
	s_waitcnt lgkmcnt(4)
	v_add_f32_e32 v19, v24, v25
	v_max3_f32 v4, v4, v18, v19
	s_waitcnt lgkmcnt(3)
	v_add_f32_e32 v14, v26, v27
	s_waitcnt lgkmcnt(2)
	v_add_f32_e32 v13, v28, v30
	s_waitcnt lgkmcnt(0)
	v_add_f32_e32 v32, v32, v33
	v_max3_f32 v4, v4, v14, v13
	v_add_f32_e32 v10, v29, v31
	v_max3_f32 v12, v4, v10, v32
	v_sub_f32_e32 v4, v32, v12
	v_mul_f32_e32 v9, 0x3fb8aa3b, v4
	v_fma_f32 v20, v4, s58, -v9
	v_rndne_f32_e32 v21, v9
	v_fmac_f32_e32 v20, 0x32a5705f, v4
	v_sub_f32_e32 v9, v9, v21
	v_add_f32_e32 v9, v9, v20
	v_exp_f32_e32 v9, v9
	v_cvt_i32_f32_e32 v20, v21
	v_cmp_ngt_f32_e32 vcc, s59, v4
	v_sub_f32_e32 v2, v2, v12
	v_sub_f32_e32 v3, v3, v12
	v_ldexp_f32 v9, v9, v20
	v_cndmask_b32_e32 v9, 0, v9, vcc
	v_cmp_nlt_f32_e32 vcc, s60, v4
	v_mul_f32_e32 v4, 0x3fb8aa3b, v2
	v_fma_f32 v20, v2, s58, -v4
	v_rndne_f32_e32 v21, v4
	v_fmac_f32_e32 v20, 0x32a5705f, v2
	v_sub_f32_e32 v4, v4, v21
	v_add_f32_e32 v4, v4, v20
	v_exp_f32_e32 v4, v4
	v_cvt_i32_f32_e32 v20, v21
	v_cndmask_b32_e32 v9, v209, v9, vcc
	v_cmp_ngt_f32_e32 vcc, s59, v2
	v_sub_f32_e32 v17, v17, v12
	v_ldexp_f32 v4, v4, v20
	v_cndmask_b32_e32 v4, 0, v4, vcc
	v_cmp_nlt_f32_e32 vcc, s60, v2
	v_sub_f32_e32 v18, v18, v12
	v_sub_f32_e32 v19, v19, v12
	v_cndmask_b32_e32 v2, v209, v4, vcc
	v_mul_f32_e32 v4, 0x3fb8aa3b, v3
	v_fma_f32 v20, v3, s58, -v4
	v_rndne_f32_e32 v21, v4
	v_fmac_f32_e32 v20, 0x32a5705f, v3
	v_sub_f32_e32 v4, v4, v21
	v_add_f32_e32 v4, v4, v20
	v_exp_f32_e32 v4, v4
	v_cvt_i32_f32_e32 v20, v21
	v_cmp_ngt_f32_e32 vcc, s59, v3
	v_sub_f32_e32 v14, v14, v12
	v_sub_f32_e32 v13, v13, v12
	v_ldexp_f32 v4, v4, v20
	v_cndmask_b32_e32 v4, 0, v4, vcc
	v_cmp_nlt_f32_e32 vcc, s60, v3
	v_sub_f32_e32 v10, v10, v12
	s_nop 0
	v_cndmask_b32_e32 v3, v209, v4, vcc
	v_sub_f32_e32 v4, v5, v12
	v_mul_f32_e32 v5, 0x3fb8aa3b, v4
	v_fma_f32 v21, v4, s58, -v5
	v_rndne_f32_e32 v22, v5
	v_fmac_f32_e32 v21, 0x32a5705f, v4
	v_sub_f32_e32 v5, v5, v22
	v_add_f32_e32 v5, v5, v21
	v_exp_f32_e32 v5, v5
	v_cvt_i32_f32_e32 v21, v22
	v_cmp_ngt_f32_e32 vcc, s59, v4
	v_add_f32_e32 v20, v2, v3
	v_ldexp_f32 v5, v5, v21
	v_cndmask_b32_e32 v5, 0, v5, vcc
	v_cmp_nlt_f32_e32 vcc, s60, v4
	s_nop 1
	v_cndmask_b32_e32 v4, v209, v5, vcc
	v_sub_f32_e32 v5, v6, v12
	v_mul_f32_e32 v6, 0x3fb8aa3b, v5
	v_fma_f32 v21, v5, s58, -v6
	v_rndne_f32_e32 v22, v6
	v_fmac_f32_e32 v21, 0x32a5705f, v5
	v_sub_f32_e32 v6, v6, v22
	v_add_f32_e32 v6, v6, v21
	v_exp_f32_e32 v6, v6
	v_cvt_i32_f32_e32 v21, v22
	v_cmp_ngt_f32_e32 vcc, s59, v5
	v_add_f32_e32 v20, v4, v20
	v_ldexp_f32 v6, v6, v21
	v_cndmask_b32_e32 v6, 0, v6, vcc
	v_cmp_nlt_f32_e32 vcc, s60, v5
	s_nop 1
	v_cndmask_b32_e32 v5, v209, v6, vcc
	v_sub_f32_e32 v6, v7, v12
	v_mul_f32_e32 v7, 0x3fb8aa3b, v6
	v_fma_f32 v21, v6, s58, -v7
	v_rndne_f32_e32 v22, v7
	v_fmac_f32_e32 v21, 0x32a5705f, v6
	v_sub_f32_e32 v7, v7, v22
	v_add_f32_e32 v7, v7, v21
	v_exp_f32_e32 v7, v7
	v_cvt_i32_f32_e32 v21, v22
	v_cmp_ngt_f32_e32 vcc, s59, v6
	v_add_f32_e32 v20, v5, v20
	v_ldexp_f32 v7, v7, v21
	v_cndmask_b32_e32 v7, 0, v7, vcc
	v_cmp_nlt_f32_e32 vcc, s60, v6
	s_nop 1
	v_cndmask_b32_e32 v6, v209, v7, vcc
	v_sub_f32_e32 v7, v8, v12
	v_mul_f32_e32 v8, 0x3fb8aa3b, v7
	v_fma_f32 v21, v7, s58, -v8
	v_rndne_f32_e32 v22, v8
	v_fmac_f32_e32 v21, 0x32a5705f, v7
	v_sub_f32_e32 v8, v8, v22
	v_add_f32_e32 v8, v8, v21
	v_exp_f32_e32 v8, v8
	v_cvt_i32_f32_e32 v21, v22
	v_cmp_ngt_f32_e32 vcc, s59, v7
	v_add_f32_e32 v20, v6, v20
	v_ldexp_f32 v8, v8, v21
	v_cndmask_b32_e32 v8, 0, v8, vcc
	v_cmp_nlt_f32_e32 vcc, s60, v7
	s_nop 1
	v_cndmask_b32_e32 v7, v209, v8, vcc
	v_sub_f32_e32 v8, v11, v12
	v_mul_f32_e32 v11, 0x3fb8aa3b, v8
	v_fma_f32 v21, v8, s58, -v11
	v_rndne_f32_e32 v22, v11
	v_fmac_f32_e32 v21, 0x32a5705f, v8
	v_sub_f32_e32 v11, v11, v22
	v_add_f32_e32 v11, v11, v21
	v_exp_f32_e32 v11, v11
	v_cvt_i32_f32_e32 v21, v22
	v_cmp_ngt_f32_e32 vcc, s59, v8
	v_add_f32_e32 v20, v7, v20
	v_ldexp_f32 v11, v11, v21
	v_cndmask_b32_e32 v11, 0, v11, vcc
	v_cmp_nlt_f32_e32 vcc, s60, v8
	s_nop 1
	v_cndmask_b32_e32 v8, v209, v11, vcc
	v_sub_f32_e32 v11, v15, v12
	v_mul_f32_e32 v15, 0x3fb8aa3b, v11
	v_fma_f32 v21, v11, s58, -v15
	v_rndne_f32_e32 v22, v15
	v_fmac_f32_e32 v21, 0x32a5705f, v11
	v_sub_f32_e32 v15, v15, v22
	v_add_f32_e32 v15, v15, v21
	v_exp_f32_e32 v15, v15
	v_cvt_i32_f32_e32 v21, v22
	v_cmp_ngt_f32_e32 vcc, s59, v11
	v_add_f32_e32 v20, v8, v20
	v_ldexp_f32 v15, v15, v21
	v_cndmask_b32_e32 v15, 0, v15, vcc
	v_cmp_nlt_f32_e32 vcc, s60, v11
	s_nop 1
	v_cndmask_b32_e32 v11, v209, v15, vcc
	v_sub_f32_e32 v15, v16, v12
	v_mul_f32_e32 v16, 0x3fb8aa3b, v15
	v_fma_f32 v21, v15, s58, -v16
	v_rndne_f32_e32 v22, v16
	v_fmac_f32_e32 v21, 0x32a5705f, v15
	v_sub_f32_e32 v16, v16, v22
	v_add_f32_e32 v16, v16, v21
	v_exp_f32_e32 v16, v16
	v_cvt_i32_f32_e32 v21, v22
	v_cmp_ngt_f32_e32 vcc, s59, v15
	v_add_f32_e32 v20, v11, v20
	v_mul_f32_e32 v12, 0x3fb8aa3b, v10
	v_ldexp_f32 v16, v16, v21
	v_cndmask_b32_e32 v16, 0, v16, vcc
	v_cmp_nlt_f32_e32 vcc, s60, v15
	s_nop 1
	v_cndmask_b32_e32 v15, v209, v16, vcc
	v_add_f32_e32 v16, v15, v20
	v_mul_f32_e32 v20, 0x3fb8aa3b, v17
	v_fma_f32 v21, v17, s58, -v20
	v_rndne_f32_e32 v22, v20
	v_fmac_f32_e32 v21, 0x32a5705f, v17
	v_sub_f32_e32 v20, v20, v22
	v_add_f32_e32 v20, v20, v21
	v_exp_f32_e32 v20, v20
	v_cvt_i32_f32_e32 v21, v22
	v_cmp_ngt_f32_e32 vcc, s59, v17
	v_ldexp_f32 v20, v20, v21
	s_nop 0
	v_cndmask_b32_e32 v20, 0, v20, vcc
	v_cmp_nlt_f32_e32 vcc, s60, v17
	s_nop 1
	v_cndmask_b32_e32 v17, v209, v20, vcc
	v_mul_f32_e32 v20, 0x3fb8aa3b, v18
	v_fma_f32 v21, v18, s58, -v20
	v_rndne_f32_e32 v22, v20
	v_fmac_f32_e32 v21, 0x32a5705f, v18
	v_sub_f32_e32 v20, v20, v22
	v_add_f32_e32 v20, v20, v21
	v_exp_f32_e32 v20, v20
	v_cvt_i32_f32_e32 v21, v22
	v_cmp_ngt_f32_e32 vcc, s59, v18
	v_add_f32_e32 v16, v17, v16
	v_ldexp_f32 v20, v20, v21
	v_cndmask_b32_e32 v20, 0, v20, vcc
	v_cmp_nlt_f32_e32 vcc, s60, v18
	s_nop 1
	v_cndmask_b32_e32 v18, v209, v20, vcc
	v_mul_f32_e32 v20, 0x3fb8aa3b, v19
	v_fma_f32 v21, v19, s58, -v20
	v_rndne_f32_e32 v22, v20
	v_fmac_f32_e32 v21, 0x32a5705f, v19
	v_sub_f32_e32 v20, v20, v22
	v_add_f32_e32 v20, v20, v21
	v_exp_f32_e32 v20, v20
	v_cvt_i32_f32_e32 v21, v22
	v_cmp_ngt_f32_e32 vcc, s59, v19
	v_add_f32_e32 v16, v18, v16
	v_ldexp_f32 v20, v20, v21
	v_cndmask_b32_e32 v20, 0, v20, vcc
	v_cmp_nlt_f32_e32 vcc, s60, v19
	s_nop 1
	v_cndmask_b32_e32 v19, v209, v20, vcc
	v_mul_f32_e32 v20, 0x3fb8aa3b, v14
	v_fma_f32 v21, v14, s58, -v20
	v_rndne_f32_e32 v22, v20
	v_fmac_f32_e32 v21, 0x32a5705f, v14
	v_sub_f32_e32 v20, v20, v22
	v_add_f32_e32 v20, v20, v21
	v_exp_f32_e32 v20, v20
	v_cvt_i32_f32_e32 v21, v22
	v_cmp_ngt_f32_e32 vcc, s59, v14
	v_add_f32_e32 v16, v19, v16
	v_ldexp_f32 v20, v20, v21
	v_cndmask_b32_e32 v20, 0, v20, vcc
	v_cmp_nlt_f32_e32 vcc, s60, v14
	s_nop 1
	v_cndmask_b32_e32 v14, v209, v20, vcc
	v_mul_f32_e32 v20, 0x3fb8aa3b, v13
	v_fma_f32 v21, v13, s58, -v20
	v_rndne_f32_e32 v22, v20
	v_fmac_f32_e32 v21, 0x32a5705f, v13
	v_sub_f32_e32 v20, v20, v22
	v_add_f32_e32 v20, v20, v21
	v_exp_f32_e32 v20, v20
	v_cvt_i32_f32_e32 v21, v22
	v_cmp_ngt_f32_e32 vcc, s59, v13
	v_add_f32_e32 v16, v14, v16
	v_ldexp_f32 v20, v20, v21
	v_cndmask_b32_e32 v20, 0, v20, vcc
	v_cmp_nlt_f32_e32 vcc, s60, v13
	v_rndne_f32_e32 v21, v12
	s_nop 0
	v_cndmask_b32_e32 v13, v209, v20, vcc
	v_fma_f32 v20, v10, s58, -v12
	v_fmac_f32_e32 v20, 0x32a5705f, v10
	v_sub_f32_e32 v12, v12, v21
	v_add_f32_e32 v12, v12, v20
	v_exp_f32_e32 v12, v12
	v_cvt_i32_f32_e32 v20, v21
	v_cmp_ngt_f32_e32 vcc, s59, v10
	v_add_f32_e32 v16, v13, v16
	v_ldexp_f32 v12, v12, v20
	v_cndmask_b32_e32 v12, 0, v12, vcc
	v_cmp_nlt_f32_e32 vcc, s60, v10
	s_nop 1
	v_cndmask_b32_e32 v12, v209, v12, vcc
	v_add_f32_e32 v10, v12, v16
	v_add_f32_e32 v10, v9, v10
	v_div_scale_f32 v16, s[62:63], v10, v10, v9
	v_rcp_f32_e32 v20, v16
	s_nop 0
	v_fma_f32 v21, -v16, v20, 1.0
	v_fmac_f32_e32 v20, v21, v20
	v_div_scale_f32 v21, vcc, v9, v10, v9
	v_mul_f32_e32 v22, v21, v20
	v_fma_f32 v23, -v16, v22, v21
	v_fmac_f32_e32 v22, v23, v20
	v_fma_f32 v16, -v16, v22, v21
	v_div_fmas_f32 v16, v16, v20, v22
	v_div_fixup_f32 v9, v16, v10, v9
	v_div_scale_f32 v16, s[62:63], v10, v10, v12
	v_rcp_f32_e32 v20, v16
	s_nop 0
	v_fma_f32 v21, -v16, v20, 1.0
	v_fmac_f32_e32 v20, v21, v20
	v_div_scale_f32 v21, vcc, v12, v10, v12
	v_mul_f32_e32 v22, v21, v20
	v_fma_f32 v23, -v16, v22, v21
	v_fmac_f32_e32 v22, v23, v20
	v_fma_f32 v16, -v16, v22, v21
	v_div_fmas_f32 v16, v16, v20, v22
	v_div_fixup_f32 v12, v16, v10, v12
	v_div_scale_f32 v16, s[62:63], v10, v10, v13
	v_rcp_f32_e32 v20, v16
	s_nop 0
	v_fma_f32 v21, -v16, v20, 1.0
	v_fmac_f32_e32 v20, v21, v20
	v_div_scale_f32 v21, vcc, v13, v10, v13
	v_mul_f32_e32 v22, v21, v20
	v_fma_f32 v23, -v16, v22, v21
	v_fmac_f32_e32 v22, v23, v20
	v_fma_f32 v16, -v16, v22, v21
	v_div_fmas_f32 v16, v16, v20, v22
	v_div_fixup_f32 v13, v16, v10, v13
	v_div_scale_f32 v16, s[62:63], v10, v10, v14
	v_rcp_f32_e32 v20, v16
	s_nop 0
	v_fma_f32 v21, -v16, v20, 1.0
	v_fmac_f32_e32 v20, v21, v20
	v_div_scale_f32 v21, vcc, v14, v10, v14
	v_mul_f32_e32 v22, v21, v20
	v_fma_f32 v23, -v16, v22, v21
	v_fmac_f32_e32 v22, v23, v20
	v_fma_f32 v16, -v16, v22, v21
	v_div_fmas_f32 v16, v16, v20, v22
	v_div_fixup_f32 v14, v16, v10, v14
	v_div_scale_f32 v16, s[62:63], v10, v10, v19
	v_rcp_f32_e32 v20, v16
	s_nop 0
	v_fma_f32 v21, -v16, v20, 1.0
	v_fmac_f32_e32 v20, v21, v20
	v_div_scale_f32 v21, vcc, v19, v10, v19
	v_mul_f32_e32 v22, v21, v20
	v_fma_f32 v23, -v16, v22, v21
	v_fmac_f32_e32 v22, v23, v20
	v_fma_f32 v16, -v16, v22, v21
	v_div_fmas_f32 v16, v16, v20, v22
	v_div_fixup_f32 v16, v16, v10, v19
	v_div_scale_f32 v19, s[62:63], v10, v10, v18
	v_rcp_f32_e32 v20, v19
	s_nop 0
	v_fma_f32 v21, -v19, v20, 1.0
	v_fmac_f32_e32 v20, v21, v20
	v_div_scale_f32 v21, vcc, v18, v10, v18
	v_mul_f32_e32 v22, v21, v20
	v_fma_f32 v23, -v19, v22, v21
	v_fmac_f32_e32 v22, v23, v20
	v_fma_f32 v19, -v19, v22, v21
	v_div_fmas_f32 v19, v19, v20, v22
	v_div_fixup_f32 v18, v19, v10, v18
	v_div_scale_f32 v19, s[62:63], v10, v10, v17
	v_rcp_f32_e32 v20, v19
	s_nop 0
	v_fma_f32 v21, -v19, v20, 1.0
	v_fmac_f32_e32 v20, v21, v20
	v_div_scale_f32 v21, vcc, v17, v10, v17
	v_mul_f32_e32 v22, v21, v20
	v_fma_f32 v23, -v19, v22, v21
	v_fmac_f32_e32 v22, v23, v20
	v_fma_f32 v19, -v19, v22, v21
	v_div_fmas_f32 v19, v19, v20, v22
	v_div_fixup_f32 v17, v19, v10, v17
	v_div_scale_f32 v19, s[62:63], v10, v10, v15
	v_rcp_f32_e32 v20, v19
	s_nop 0
	v_fma_f32 v21, -v19, v20, 1.0
	v_fmac_f32_e32 v20, v21, v20
	v_div_scale_f32 v21, vcc, v15, v10, v15
	v_mul_f32_e32 v22, v21, v20
	v_fma_f32 v23, -v19, v22, v21
	v_fmac_f32_e32 v22, v23, v20
	v_fma_f32 v19, -v19, v22, v21
	v_div_fmas_f32 v19, v19, v20, v22
	v_div_fixup_f32 v15, v19, v10, v15
	v_div_scale_f32 v19, s[62:63], v10, v10, v11
	v_rcp_f32_e32 v20, v19
	s_nop 0
	v_fma_f32 v21, -v19, v20, 1.0
	v_fmac_f32_e32 v20, v21, v20
	v_div_scale_f32 v21, vcc, v11, v10, v11
	v_mul_f32_e32 v22, v21, v20
	v_fma_f32 v23, -v19, v22, v21
	v_fmac_f32_e32 v22, v23, v20
	v_fma_f32 v19, -v19, v22, v21
	v_div_fmas_f32 v19, v19, v20, v22
	v_div_fixup_f32 v11, v19, v10, v11
	v_div_scale_f32 v19, s[62:63], v10, v10, v8
	v_rcp_f32_e32 v20, v19
	s_nop 0
	v_fma_f32 v21, -v19, v20, 1.0
	v_fmac_f32_e32 v20, v21, v20
	v_div_scale_f32 v21, vcc, v8, v10, v8
	v_mul_f32_e32 v22, v21, v20
	v_fma_f32 v23, -v19, v22, v21
	v_fmac_f32_e32 v22, v23, v20
	v_fma_f32 v19, -v19, v22, v21
	v_div_fmas_f32 v19, v19, v20, v22
	v_div_fixup_f32 v8, v19, v10, v8
	v_div_scale_f32 v19, s[62:63], v10, v10, v7
	v_rcp_f32_e32 v20, v19
	s_nop 0
	v_fma_f32 v21, -v19, v20, 1.0
	v_fmac_f32_e32 v20, v21, v20
	v_div_scale_f32 v21, vcc, v7, v10, v7
	v_mul_f32_e32 v22, v21, v20
	v_fma_f32 v23, -v19, v22, v21
	v_fmac_f32_e32 v22, v23, v20
	v_fma_f32 v19, -v19, v22, v21
	v_div_fmas_f32 v19, v19, v20, v22
	v_div_fixup_f32 v7, v19, v10, v7
	v_div_scale_f32 v19, s[62:63], v10, v10, v6
	v_rcp_f32_e32 v20, v19
	s_nop 0
	v_fma_f32 v21, -v19, v20, 1.0
	v_fmac_f32_e32 v20, v21, v20
	v_div_scale_f32 v21, vcc, v6, v10, v6
	v_mul_f32_e32 v22, v21, v20
	v_fma_f32 v23, -v19, v22, v21
	v_fmac_f32_e32 v22, v23, v20
	v_fma_f32 v19, -v19, v22, v21
	v_div_fmas_f32 v19, v19, v20, v22
	v_div_fixup_f32 v6, v19, v10, v6
	v_div_scale_f32 v19, s[62:63], v10, v10, v5
	v_rcp_f32_e32 v20, v19
	s_nop 0
	v_fma_f32 v21, -v19, v20, 1.0
	v_fmac_f32_e32 v20, v21, v20
	v_div_scale_f32 v21, vcc, v5, v10, v5
	v_mul_f32_e32 v22, v21, v20
	v_fma_f32 v23, -v19, v22, v21
	v_fmac_f32_e32 v22, v23, v20
	v_fma_f32 v19, -v19, v22, v21
	v_div_fmas_f32 v19, v19, v20, v22
	v_div_fixup_f32 v5, v19, v10, v5
	v_div_scale_f32 v19, s[62:63], v10, v10, v4
	v_rcp_f32_e32 v20, v19
	s_nop 0
	v_fma_f32 v21, -v19, v20, 1.0
	v_fmac_f32_e32 v20, v21, v20
	v_div_scale_f32 v21, vcc, v4, v10, v4
	v_mul_f32_e32 v22, v21, v20
	v_fma_f32 v23, -v19, v22, v21
	v_fmac_f32_e32 v22, v23, v20
	v_fma_f32 v19, -v19, v22, v21
	v_div_fmas_f32 v19, v19, v20, v22
	v_div_fixup_f32 v4, v19, v10, v4
	v_div_scale_f32 v19, s[62:63], v10, v10, v3
	v_rcp_f32_e32 v20, v19
	s_nop 0
	v_fma_f32 v21, -v19, v20, 1.0
	v_fmac_f32_e32 v20, v21, v20
	v_div_scale_f32 v21, vcc, v3, v10, v3
	v_mul_f32_e32 v22, v21, v20
	v_fma_f32 v23, -v19, v22, v21
	v_fmac_f32_e32 v22, v23, v20
	v_fma_f32 v19, -v19, v22, v21
	v_div_fmas_f32 v19, v19, v20, v22
	v_div_fixup_f32 v3, v19, v10, v3
	v_div_scale_f32 v19, s[62:63], v10, v10, v2
	v_rcp_f32_e32 v20, v19
	s_nop 0
	v_fma_f32 v21, -v19, v20, 1.0
	v_fmac_f32_e32 v20, v21, v20
	v_div_scale_f32 v21, vcc, v2, v10, v2
	v_mul_f32_e32 v22, v21, v20
	v_fma_f32 v23, -v19, v22, v21
	v_fmac_f32_e32 v22, v23, v20
	v_fma_f32 v19, -v19, v22, v21
	v_div_fmas_f32 v19, v19, v20, v22
	v_div_fixup_f32 v2, v19, v10, v2
	v_cndmask_b32_e64 v2, 0, v2, s[36:37]
	v_cndmask_b32_e64 v2, v2, v3, s[34:35]
	v_cndmask_b32_e64 v2, v2, v4, s[30:31]
	v_cndmask_b32_e64 v2, v2, v5, s[28:29]
	v_cndmask_b32_e64 v2, v2, v6, s[26:27]
	v_cndmask_b32_e64 v2, v2, v7, s[24:25]
	v_cndmask_b32_e64 v2, v2, v8, s[22:23]
	v_cndmask_b32_e64 v2, v2, v11, s[20:21]
	v_cndmask_b32_e64 v2, v2, v15, s[18:19]
	v_cndmask_b32_e64 v2, v2, v17, s[16:17]
	v_cndmask_b32_e64 v2, v2, v18, s[14:15]
	v_cndmask_b32_e64 v2, v2, v16, s[12:13]
	v_cndmask_b32_e64 v2, v2, v14, s[10:11]
	v_cndmask_b32_e64 v2, v2, v13, s[8:9]
	v_cndmask_b32_e64 v2, v2, v12, s[6:7]
	v_cndmask_b32_e64 v4, v2, v9, s[4:5]
	v_lshl_add_u64 v[2:3], s[40:41], 0, v[106:107]
	global_store_dword v[2:3], v4, off
	s_branch .LBB0_1364
